# loop-edge edit: the five GEMM K-loops run their loop-carried scalar bumps and exit compare before the last barrier of the iteration
# baseline (speedup 1.0000x reference)
; #define PG8_STAGE(bufoff, gbase, voff) do { _Pragma("unroll") for (int _i = 0; _i < 2; ++_i) \
;         __builtin_amdgcn_global_load_lds((const unsigned*)((const char*)(gbase) + (voff)[_i]), (PG8_LAS unsigned*)(lds + (bufoff) + ldsw + _i * 8192), 16, 0, 0); } while (0)
; #define PG8_LDA(dst, b, h) do { _Pragma("unroll") for (int m = 0; m < 4; ++m) _Pragma("unroll") for (int k = 0; k < 2; ++k) dst[m][k] = *(const PG8_LAS bf16x8*)(lds + PG8_SA(b, h) + aoff + m * 2048 + k * 1024); } while (0)
; #define PG8_LDB(dst, b, h) do { _Pragma("unroll") for (int n = 0; n < 2; ++n) _Pragma("unroll") for (int k = 0; k < 2; ++k) dst[n][k] = *(const PG8_LAS bf16x8*)(lds + PG8_SB(b, h) + boff + n * 2048 + k * 1024); } while (0)
; #define PG8_WAIT_V(n) asm volatile("s_waitcnt vmcnt(" #n ")" ::: "memory")
; #define PG8_WAIT_L(n) asm volatile("s_waitcnt lgkmcnt(" #n ")" ::: "memory")
; #define PG8_BAR __builtin_amdgcn_s_barrier()
; #define PG8_SCHED __builtin_amdgcn_sched_barrier(0)
;     ...
;             const bool last = (t == nt - 2);
;             const char* a1 = cA + (size_t)(t + 1) * kstep;
;             const char* a2 = last ? nA : cA + (size_t)(t + 2) * kstep; const char* b2 = last ? nB : cB + (size_t)(t + 2) * kstep;
;             const char* a3 = a2 + kstep; const char* b3 = b2 + kstep;
;             if (last && has_next) S.a_ready(nxt);
;             if constexpr (Epi::MIDK > 0) { if (t == Epi::MIDK) {
;                 if constexpr (FP8) asm volatile("s_nop 15\n\ts_nop 15" ::: "memory");
;                 E.mid(acc, cur, wr, wc, fr, fq);
;                 if constexpr (FP8) asm volatile("s_nop 7" ::: "memory"); } }
;             if constexpr (SP2) {
;             PG8_LDB(B0, 0, 0); PG8_LDB(B1, 0, 1); PG8_SCHED; PG8_LDA(At, 0, 0); PG8_STAGE(PG8_SA(1, 1), a1 + hstepA, voffA);
;             PG8_WAIT_V(8); PG8_WAIT_L(0); PG8_BAR; PG8_MMA(0, 0, At, B0); PG8_MMA(0, 1, At, B1); PG8_BAR; PG8_SCHED;
;             PG8_LDA(At, 0, 1); PG8_STAGE(PG8_SB(0, 0), b2, voffB); PG8_STAGE(PG8_SB(0, 1), b2 + hstepB, voffB); PG8_STAGE(PG8_SA(0, 0), a2, voffA);
;             PG8_WAIT_V(8); PG8_WAIT_L(0); PG8_BAR; PG8_MMA(1, 0, At, B0); PG8_MMA(1, 1, At, B1); PG8_BAR; PG8_SCHED;
.LBB0_177:
	ds_read_b128 v[26:29], v200
	ds_read_b128 v[30:33], v200 offset:1024
	s_waitcnt vmcnt(0)
	ds_read_b128 v[18:21], v200 offset:2048
	ds_read_b128 v[22:25], v200 offset:3072
	ds_read_b128 v[10:13], v201
	ds_read_b128 v[14:17], v201 offset:1024
	ds_read_b128 v[2:5], v201 offset:2048
	ds_read_b128 v[6:9], v201 offset:3072
	s_add_u32 s90, s88, 0xfff80080
	s_addc_u32 s91, s89, -1
	s_cmp_eq_u32 s83, 28
	s_cselect_b32 s93, s0, s91
	s_cselect_b32 s92, s1, s90
	s_cselect_b32 s91, s7, s49
	s_cselect_b32 s90, s9, s37
	v_lshl_add_u64 v[232:233], s[88:89], 0, v[170:171]
	s_add_i32 m0, s45, 0xc000
	ds_read_b128 v[178:181], v202
	ds_read_b128 v[182:185], v202 offset:1024
	ds_read_b128 v[208:211], v202 offset:2048
	ds_read_b128 v[212:215], v202 offset:3072
	ds_read_b128 v[216:219], v202 offset:4096
	ds_read_b128 v[220:223], v202 offset:5120
	ds_read_b128 v[224:227], v202 offset:6144
	ds_read_b128 v[228:231], v202 offset:7168
	global_load_lds_dwordx4 v[232:233], off
	v_lshl_add_u64 v[232:233], s[88:89], 0, v[172:173]
	s_add_i32 m0, s45, 0xe000
	s_nop 0
	global_load_lds_dwordx4 v[232:233], off
	s_waitcnt vmcnt(8)
	s_waitcnt lgkmcnt(0)
	s_barrier
	s_setprio 1
	s_waitcnt lgkmcnt(0)
	v_mfma_scale_f32_16x16x128_f8f6f4 v[158:161], v[26:33], v[178:185], v[158:161], v203, v203 op_sel_hi:[0,0,0]
	v_mfma_scale_f32_16x16x128_f8f6f4 v[154:157], v[18:25], v[178:185], v[154:157], v203, v203 op_sel_hi:[0,0,0]
	v_mfma_scale_f32_16x16x128_f8f6f4 v[142:145], v[26:33], v[208:215], v[142:145], v203, v203 op_sel_hi:[0,0,0]
	v_mfma_scale_f32_16x16x128_f8f6f4 v[138:141], v[18:25], v[208:215], v[138:141], v203, v203 op_sel_hi:[0,0,0]
	v_mfma_scale_f32_16x16x128_f8f6f4 v[126:129], v[26:33], v[216:223], v[126:129], v203, v203 op_sel_hi:[0,0,0]
	v_mfma_scale_f32_16x16x128_f8f6f4 v[122:125], v[18:25], v[216:223], v[122:125], v203, v203 op_sel_hi:[0,0,0]
	v_mfma_scale_f32_16x16x128_f8f6f4 v[110:113], v[26:33], v[224:231], v[110:113], v203, v203 op_sel_hi:[0,0,0]
	v_mfma_scale_f32_16x16x128_f8f6f4 v[106:109], v[18:25], v[224:231], v[106:109], v203, v203 op_sel_hi:[0,0,0]
	s_setprio 0
	s_setprio 1
	v_mfma_scale_f32_16x16x128_f8f6f4 v[150:153], v[10:17], v[178:185], v[150:153], v203, v203 op_sel_hi:[0,0,0]
	v_mfma_scale_f32_16x16x128_f8f6f4 v[146:149], v[2:9], v[178:185], v[146:149], v203, v203 op_sel_hi:[0,0,0]
	v_mfma_scale_f32_16x16x128_f8f6f4 v[134:137], v[10:17], v[208:215], v[134:137], v203, v203 op_sel_hi:[0,0,0]
	v_mfma_scale_f32_16x16x128_f8f6f4 v[130:133], v[2:9], v[208:215], v[130:133], v203, v203 op_sel_hi:[0,0,0]
	v_mfma_scale_f32_16x16x128_f8f6f4 v[118:121], v[10:17], v[216:223], v[118:121], v203, v203 op_sel_hi:[0,0,0]
	v_mfma_scale_f32_16x16x128_f8f6f4 v[114:117], v[2:9], v[216:223], v[114:117], v203, v203 op_sel_hi:[0,0,0]
	v_mfma_scale_f32_16x16x128_f8f6f4 v[102:105], v[10:17], v[224:231], v[102:105], v203, v203 op_sel_hi:[0,0,0]
	v_mfma_scale_f32_16x16x128_f8f6f4 v[98:101], v[2:9], v[224:231], v[98:101], v203, v203 op_sel_hi:[0,0,0]
	s_setprio 0
	s_barrier
	s_add_i32 vcc_lo, s95, s42
	v_lshl_add_u64 v[178:179], s[90:91], 0, v[164:165]
	s_mov_b32 m0, vcc_lo
	ds_read_b128 v[208:211], v202 offset:16384
	ds_read_b128 v[212:215], v202 offset:17408
	ds_read_b128 v[216:219], v202 offset:18432
	ds_read_b128 v[220:223], v202 offset:19456
	ds_read_b128 v[224:227], v202 offset:20480
	ds_read_b128 v[228:231], v202 offset:21504
	ds_read_b128 v[232:235], v202 offset:22528
	ds_read_b128 v[236:239], v202 offset:23552
	global_load_lds_dwordx4 v[178:179], off
	s_add_i32 m0, vcc_lo, 0x2000
	s_add_u32 vcc_lo, s90, 0x80000
	v_lshl_add_u64 v[180:181], s[90:91], 0, v[168:169]
	s_addc_u32 vcc_hi, s91, 0
	s_add_i32 s20, s14, s42
	global_load_lds_dwordx4 v[180:181], off
	v_lshl_add_u64 v[182:183], vcc, 0, v[164:165]
	s_mov_b32 m0, s20
	v_lshl_add_u64 v[184:185], s[92:93], 0, v[166:167]
	global_load_lds_dwordx4 v[182:183], off
	v_lshl_add_u64 v[182:183], vcc, 0, v[168:169]
	s_add_i32 m0, s20, 0x2000
	s_nop 0
	global_load_lds_dwordx4 v[182:183], off
	v_lshl_add_u64 v[182:183], s[92:93], 0, v[162:163]
	s_mov_b32 m0, s45
	s_nop 0
	global_load_lds_dwordx4 v[182:183], off
	s_mov_b32 m0, s46
	s_nop 0
	global_load_lds_dwordx4 v[184:185], off
	s_waitcnt vmcnt(8)
	s_waitcnt lgkmcnt(0)
	s_barrier
	s_setprio 1
	s_waitcnt lgkmcnt(0)
	v_mfma_scale_f32_16x16x128_f8f6f4 v[94:97], v[26:33], v[208:215], v[94:97], v203, v203 op_sel_hi:[0,0,0]
	v_mfma_scale_f32_16x16x128_f8f6f4 v[90:93], v[18:25], v[208:215], v[90:93], v203, v203 op_sel_hi:[0,0,0]
	v_mfma_scale_f32_16x16x128_f8f6f4 v[78:81], v[26:33], v[216:223], v[78:81], v203, v203 op_sel_hi:[0,0,0]
	v_mfma_scale_f32_16x16x128_f8f6f4 v[74:77], v[18:25], v[216:223], v[74:77], v203, v203 op_sel_hi:[0,0,0]
	v_mfma_scale_f32_16x16x128_f8f6f4 v[62:65], v[26:33], v[224:231], v[62:65], v203, v203 op_sel_hi:[0,0,0]
	v_mfma_scale_f32_16x16x128_f8f6f4 v[58:61], v[18:25], v[224:231], v[58:61], v203, v203 op_sel_hi:[0,0,0]
	v_mfma_scale_f32_16x16x128_f8f6f4 v[46:49], v[26:33], v[232:239], v[46:49], v203, v203 op_sel_hi:[0,0,0]
	v_mfma_scale_f32_16x16x128_f8f6f4 v[42:45], v[18:25], v[232:239], v[42:45], v203, v203 op_sel_hi:[0,0,0]
	s_setprio 0
	s_setprio 1
	v_mfma_scale_f32_16x16x128_f8f6f4 v[86:89], v[10:17], v[208:215], v[86:89], v203, v203 op_sel_hi:[0,0,0]
	v_mfma_scale_f32_16x16x128_f8f6f4 v[82:85], v[2:9], v[208:215], v[82:85], v203, v203 op_sel_hi:[0,0,0]
	v_mfma_scale_f32_16x16x128_f8f6f4 v[70:73], v[10:17], v[216:223], v[70:73], v203, v203 op_sel_hi:[0,0,0]
	v_mfma_scale_f32_16x16x128_f8f6f4 v[66:69], v[2:9], v[216:223], v[66:69], v203, v203 op_sel_hi:[0,0,0]
	v_mfma_scale_f32_16x16x128_f8f6f4 v[54:57], v[10:17], v[224:231], v[54:57], v203, v203 op_sel_hi:[0,0,0]
	v_mfma_scale_f32_16x16x128_f8f6f4 v[50:53], v[2:9], v[224:231], v[50:53], v203, v203 op_sel_hi:[0,0,0]
	v_mfma_scale_f32_16x16x128_f8f6f4 v[38:41], v[10:17], v[232:239], v[38:41], v203, v203 op_sel_hi:[0,0,0]
	v_mfma_scale_f32_16x16x128_f8f6f4 v[34:37], v[2:9], v[232:239], v[34:37], v203, v203 op_sel_hi:[0,0,0]
	s_setprio 0
	s_barrier
; #define PG8_STAGE(bufoff, gbase, voff) do { _Pragma("unroll") for (int _i = 0; _i < 2; ++_i) \
;         __builtin_amdgcn_global_load_lds((const unsigned*)((const char*)(gbase) + (voff)[_i]), (PG8_LAS unsigned*)(lds + (bufoff) + ldsw + _i * 8192), 16, 0, 0); } while (0)
; #define PG8_LDA(dst, b, h) do { _Pragma("unroll") for (int m = 0; m < 4; ++m) _Pragma("unroll") for (int k = 0; k < 2; ++k) dst[m][k] = *(const PG8_LAS bf16x8*)(lds + PG8_SA(b, h) + aoff + m * 2048 + k * 1024); } while (0)
; #define PG8_WAIT_V(n) asm volatile("s_waitcnt vmcnt(" #n ")" ::: "memory")
; #define PG8_BAR __builtin_amdgcn_s_barrier()
;     ...
;         for (int t = 0; t < nt; t += 2) {
;             const bool last = (t == nt - 2);
;             const char* a1 = cA + (size_t)(t + 1) * kstep;
;             const char* a2 = last ? nA : cA + (size_t)(t + 2) * kstep; const char* b2 = last ? nB : cB + (size_t)(t + 2) * kstep;
;             const char* a3 = a2 + kstep; const char* b3 = b2 + kstep;
;             if (last && has_next) S.a_ready(nxt);
;             if constexpr (Epi::MIDK > 0) { if (t == Epi::MIDK) {
;                 if constexpr (FP8) asm volatile("s_nop 15\n\ts_nop 15" ::: "memory");
;                 E.mid(acc, cur, wr, wc, fr, fq);
;                 if constexpr (FP8) asm volatile("s_nop 7" ::: "memory"); } }
;             if constexpr (SP2) {
;             PG8_LDB(B0, 0, 0); PG8_LDB(B1, 0, 1); PG8_SCHED; PG8_LDA(At, 0, 0); PG8_STAGE(PG8_SA(1, 1), a1 + hstepA, voffA);
;             PG8_WAIT_V(8); PG8_WAIT_L(0); PG8_BAR; PG8_MMA(0, 0, At, B0); PG8_MMA(0, 1, At, B1); PG8_BAR; PG8_SCHED;
;             PG8_LDA(At, 0, 1); PG8_STAGE(PG8_SB(0, 0), b2, voffB); PG8_STAGE(PG8_SB(0, 1), b2 + hstepB, voffB); PG8_STAGE(PG8_SA(0, 0), a2, voffA);
;             PG8_WAIT_V(8); PG8_WAIT_L(0); PG8_BAR; PG8_MMA(1, 0, At, B0); PG8_MMA(1, 1, At, B1); PG8_BAR; PG8_SCHED;
;             PG8_LDB(B0, 1, 0); PG8_LDB(B1, 1, 1); PG8_SCHED; PG8_LDA(At, 1, 0); PG8_STAGE(PG8_SA(0, 1), a2 + hstepA, voffA);
;             PG8_WAIT_V(8); PG8_WAIT_L(0); PG8_BAR; PG8_MMA(0, 0, At, B0); PG8_MMA(0, 1, At, B1); PG8_BAR; PG8_SCHED;
;             PG8_LDA(At, 1, 1); PG8_STAGE(PG8_SB(1, 0), b3, voffB); PG8_STAGE(PG8_SB(1, 1), b3 + hstepB, voffB); PG8_STAGE(PG8_SA(1, 0), a3, voffA);
;             PG8_WAIT_V(8); PG8_WAIT_L(0); PG8_BAR; PG8_MMA(1, 0, At, B0); PG8_MMA(1, 1, At, B1); PG8_BAR; PG8_SCHED;
	s_add_i32 s20, 0, 0x18000
	s_add_i32 s21, 0, 0x1c000
	v_add_u32_e32 v14, s20, v199
	v_add_u32_e32 v30, s21, v199
	ds_read_b128 v[2:5], v14
	ds_read_b128 v[6:9], v14 offset:1024
	ds_read_b128 v[10:13], v14 offset:2048
	ds_read_b128 v[14:17], v14 offset:3072
	ds_read_b128 v[18:21], v30
	ds_read_b128 v[22:25], v30 offset:1024
	ds_read_b128 v[26:29], v30 offset:2048
	ds_read_b128 v[30:33], v30 offset:3072
	s_add_u32 s92, s92, 0x80000
	s_addc_u32 s93, s93, 0
	s_mov_b32 m0, s47
	v_lshl_add_u64 v[240:241], s[92:93], 0, v[162:163]
	ds_read_b128 v[208:211], v202 offset:32768
	ds_read_b128 v[212:215], v202 offset:33792
	ds_read_b128 v[216:219], v202 offset:34816
	ds_read_b128 v[220:223], v202 offset:35840
	ds_read_b128 v[224:227], v202 offset:36864
	ds_read_b128 v[228:231], v202 offset:37888
	ds_read_b128 v[232:235], v202 offset:38912
	ds_read_b128 v[236:239], v202 offset:39936
	global_load_lds_dwordx4 v[240:241], off
	v_lshl_add_u64 v[240:241], s[92:93], 0, v[166:167]
	s_mov_b32 m0, s33
	s_nop 0
	global_load_lds_dwordx4 v[240:241], off
	s_waitcnt vmcnt(8)
	s_waitcnt lgkmcnt(0)
	s_barrier
	s_setprio 1
	s_waitcnt lgkmcnt(0)
	v_mfma_scale_f32_16x16x128_f8f6f4 v[158:161], v[2:9], v[208:215], v[158:161], v203, v203 op_sel_hi:[0,0,0]
	v_mfma_scale_f32_16x16x128_f8f6f4 v[154:157], v[10:17], v[208:215], v[154:157], v203, v203 op_sel_hi:[0,0,0]
	v_mfma_scale_f32_16x16x128_f8f6f4 v[142:145], v[2:9], v[216:223], v[142:145], v203, v203 op_sel_hi:[0,0,0]
	v_mfma_scale_f32_16x16x128_f8f6f4 v[138:141], v[10:17], v[216:223], v[138:141], v203, v203 op_sel_hi:[0,0,0]
	v_mfma_scale_f32_16x16x128_f8f6f4 v[126:129], v[2:9], v[224:231], v[126:129], v203, v203 op_sel_hi:[0,0,0]
	v_mfma_scale_f32_16x16x128_f8f6f4 v[122:125], v[10:17], v[224:231], v[122:125], v203, v203 op_sel_hi:[0,0,0]
	v_mfma_scale_f32_16x16x128_f8f6f4 v[110:113], v[2:9], v[232:239], v[110:113], v203, v203 op_sel_hi:[0,0,0]
	v_mfma_scale_f32_16x16x128_f8f6f4 v[106:109], v[10:17], v[232:239], v[106:109], v203, v203 op_sel_hi:[0,0,0]
	s_setprio 0
	s_setprio 1
	v_mfma_scale_f32_16x16x128_f8f6f4 v[150:153], v[18:25], v[208:215], v[150:153], v203, v203 op_sel_hi:[0,0,0]
	v_mfma_scale_f32_16x16x128_f8f6f4 v[146:149], v[26:33], v[208:215], v[146:149], v203, v203 op_sel_hi:[0,0,0]
	v_mfma_scale_f32_16x16x128_f8f6f4 v[134:137], v[18:25], v[216:223], v[134:137], v203, v203 op_sel_hi:[0,0,0]
	v_mfma_scale_f32_16x16x128_f8f6f4 v[130:133], v[26:33], v[216:223], v[130:133], v203, v203 op_sel_hi:[0,0,0]
	v_mfma_scale_f32_16x16x128_f8f6f4 v[118:121], v[18:25], v[224:231], v[118:121], v203, v203 op_sel_hi:[0,0,0]
	v_mfma_scale_f32_16x16x128_f8f6f4 v[114:117], v[26:33], v[224:231], v[114:117], v203, v203 op_sel_hi:[0,0,0]
	v_mfma_scale_f32_16x16x128_f8f6f4 v[102:105], v[18:25], v[232:239], v[102:105], v203, v203 op_sel_hi:[0,0,0]
	v_mfma_scale_f32_16x16x128_f8f6f4 v[98:101], v[26:33], v[232:239], v[98:101], v203, v203 op_sel_hi:[0,0,0]
	s_setprio 0
	s_barrier
	s_add_i32 s20, s20, s42
	v_lshl_add_u64 v[178:179], v[178:179], 0, s[30:31]
	s_mov_b32 m0, s20
	ds_read_b128 v[208:211], v202 offset:49152
	ds_read_b128 v[212:215], v202 offset:50176
	ds_read_b128 v[216:219], v202 offset:51200
	ds_read_b128 v[220:223], v202 offset:52224
	ds_read_b128 v[224:227], v202 offset:53248
	ds_read_b128 v[228:231], v202 offset:54272
	ds_read_b128 v[232:235], v202 offset:55296
	ds_read_b128 v[236:239], v202 offset:56320
	global_load_lds_dwordx4 v[178:179], off
	s_add_i32 m0, s20, 0x2000
	s_add_u32 s90, s90, 0x80080
	v_lshl_add_u64 v[178:179], v[180:181], 0, s[30:31]
	s_addc_u32 s91, s91, 0
	s_add_i32 s20, s21, s42
	global_load_lds_dwordx4 v[178:179], off
	v_lshl_add_u64 v[178:179], s[90:91], 0, v[164:165]
	s_mov_b32 m0, s20
	s_nop 0
	global_load_lds_dwordx4 v[178:179], off
	v_lshl_add_u64 v[178:179], s[90:91], 0, v[168:169]
	s_add_i32 m0, s20, 0x2000
	s_nop 0
	global_load_lds_dwordx4 v[178:179], off
	v_lshl_add_u64 v[178:179], v[182:183], 0, s[30:31]
	s_mov_b32 m0, s11
	s_nop 0
	global_load_lds_dwordx4 v[178:179], off
	v_lshl_add_u64 v[178:179], v[184:185], 0, s[30:31]
	s_mov_b32 m0, s68
	s_nop 0
	global_load_lds_dwordx4 v[178:179], off
	s_waitcnt vmcnt(8)
	s_waitcnt lgkmcnt(0)
	s_barrier
	s_setprio 1
	s_waitcnt lgkmcnt(0)
	v_mfma_scale_f32_16x16x128_f8f6f4 v[94:97], v[2:9], v[208:215], v[94:97], v203, v203 op_sel_hi:[0,0,0]
	v_mfma_scale_f32_16x16x128_f8f6f4 v[90:93], v[10:17], v[208:215], v[90:93], v203, v203 op_sel_hi:[0,0,0]
	v_mfma_scale_f32_16x16x128_f8f6f4 v[78:81], v[2:9], v[216:223], v[78:81], v203, v203 op_sel_hi:[0,0,0]
	v_mfma_scale_f32_16x16x128_f8f6f4 v[74:77], v[10:17], v[216:223], v[74:77], v203, v203 op_sel_hi:[0,0,0]
	v_mfma_scale_f32_16x16x128_f8f6f4 v[62:65], v[2:9], v[224:231], v[62:65], v203, v203 op_sel_hi:[0,0,0]
	v_mfma_scale_f32_16x16x128_f8f6f4 v[58:61], v[10:17], v[224:231], v[58:61], v203, v203 op_sel_hi:[0,0,0]
	v_mfma_scale_f32_16x16x128_f8f6f4 v[46:49], v[2:9], v[232:239], v[46:49], v203, v203 op_sel_hi:[0,0,0]
	v_mfma_scale_f32_16x16x128_f8f6f4 v[42:45], v[10:17], v[232:239], v[42:45], v203, v203 op_sel_hi:[0,0,0]
	s_setprio 0
	s_setprio 1
	v_mfma_scale_f32_16x16x128_f8f6f4 v[86:89], v[18:25], v[208:215], v[86:89], v203, v203 op_sel_hi:[0,0,0]
	v_mfma_scale_f32_16x16x128_f8f6f4 v[82:85], v[26:33], v[208:215], v[82:85], v203, v203 op_sel_hi:[0,0,0]
	v_mfma_scale_f32_16x16x128_f8f6f4 v[70:73], v[18:25], v[216:223], v[70:73], v203, v203 op_sel_hi:[0,0,0]
	v_mfma_scale_f32_16x16x128_f8f6f4 v[66:69], v[26:33], v[216:223], v[66:69], v203, v203 op_sel_hi:[0,0,0]
	v_mfma_scale_f32_16x16x128_f8f6f4 v[54:57], v[18:25], v[224:231], v[54:57], v203, v203 op_sel_hi:[0,0,0]
	v_mfma_scale_f32_16x16x128_f8f6f4 v[50:53], v[26:33], v[224:231], v[50:53], v203, v203 op_sel_hi:[0,0,0]
	v_mfma_scale_f32_16x16x128_f8f6f4 v[38:41], v[18:25], v[232:239], v[38:41], v203, v203 op_sel_hi:[0,0,0]
	v_mfma_scale_f32_16x16x128_f8f6f4 v[34:37], v[26:33], v[232:239], v[34:37], v203, v203 op_sel_hi:[0,0,0]
	s_setprio 0
	s_add_i32 s83, s83, 2
	s_add_u32 s88, s88, 0x100
	s_addc_u32 s89, s89, 0
	s_add_u32 s37, s37, 0x100
	s_addc_u32 s49, s49, 0
	s_cmp_gt_u32 s83, 29
	s_barrier
	s_cbranch_scc0 .LBB0_177
	s_and_b64 vcc, exec, s[38:39]
	s_cbranch_vccz .LBB0_180
	s_barrier

; #define PG8_STAGE(bufoff, gbase, voff) do { _Pragma("unroll") for (int _i = 0; _i < 2; ++_i) \
;         __builtin_amdgcn_global_load_lds((const unsigned*)((const char*)(gbase) + (voff)[_i]), (PG8_LAS unsigned*)(lds + (bufoff) + ldsw + _i * 8192), 16, 0, 0); } while (0)
; #define PG8_LDA(dst, b, h) do { _Pragma("unroll") for (int m = 0; m < 4; ++m) _Pragma("unroll") for (int k = 0; k < 2; ++k) dst[m][k] = *(const PG8_LAS bf16x8*)(lds + PG8_SA(b, h) + aoff + m * 2048 + k * 1024); } while (0)
; #define PG8_LDB(dst, b, h) do { _Pragma("unroll") for (int n = 0; n < 2; ++n) _Pragma("unroll") for (int k = 0; k < 2; ++k) dst[n][k] = *(const PG8_LAS bf16x8*)(lds + PG8_SB(b, h) + boff + n * 2048 + k * 1024); } while (0)
; #define PG8_WAIT_V(n) asm volatile("s_waitcnt vmcnt(" #n ")" ::: "memory")
; #define PG8_WAIT_L(n) asm volatile("s_waitcnt lgkmcnt(" #n ")" ::: "memory")
; #define PG8_BAR __builtin_amdgcn_s_barrier()
; #define PG8_SCHED __builtin_amdgcn_sched_barrier(0)
;     ...
;             PG8_LDB(B0, 0, 0); PG8_LDB(B1, 0, 1); PG8_SCHED; PG8_LDA(At, 0, 0); PG8_STAGE(PG8_SA(1, 1), a1 + hstepA, voffA);
;             PG8_WAIT_V(8); PG8_WAIT_L(0); PG8_BAR; PG8_MMA(0, 0, At, B0); PG8_MMA(0, 1, At, B1); PG8_BAR; PG8_SCHED;
;             PG8_LDA(At, 0, 1); PG8_STAGE(PG8_SB(0, 0), b2, voffB); PG8_STAGE(PG8_SB(0, 1), b2 + hstepB, voffB); PG8_STAGE(PG8_SA(0, 0), a2, voffA);
;             PG8_WAIT_V(8); PG8_WAIT_L(0); PG8_BAR; PG8_MMA(1, 0, At, B0); PG8_MMA(1, 1, At, B1); PG8_BAR; PG8_SCHED;
.LBB0_289:
	ds_read_b128 v[158:161], v188
	ds_read_b128 v[154:157], v188 offset:1024
	ds_read_b128 v[150:153], v188 offset:2048
	ds_read_b128 v[146:149], v188 offset:3072
	ds_read_b128 v[142:145], v189
	ds_read_b128 v[138:141], v189 offset:1024
	ds_read_b128 v[134:137], v189 offset:2048
	ds_read_b128 v[130:133], v189 offset:3072
	s_add_u32 s67, s78, 0xfffc0080
	s_addc_u32 s68, s79, -1
	s_cmp_eq_u32 s66, 12
	s_cselect_b32 s83, s0, s68
	s_cselect_b32 s82, s1, s67
	s_cselect_b32 s81, s27, s63
	s_cselect_b32 s80, s31, s62
	v_lshl_add_u64 v[218:219], s[78:79], 0, v[170:171]
	s_add_i32 m0, s25, 0xc000
	ds_read_b128 v[178:181], v190
	ds_read_b128 v[182:185], v190 offset:1024
	ds_read_b128 v[194:197], v190 offset:2048
	ds_read_b128 v[198:201], v190 offset:3072
	ds_read_b128 v[202:205], v190 offset:4096
	ds_read_b128 v[206:209], v190 offset:5120
	ds_read_b128 v[210:213], v190 offset:6144
	ds_read_b128 v[214:217], v190 offset:7168
	global_load_lds_dwordx4 v[218:219], off
	v_lshl_add_u64 v[218:219], s[78:79], 0, v[172:173]
	s_add_i32 m0, s25, 0xe000
	s_nop 0
	global_load_lds_dwordx4 v[218:219], off
	s_waitcnt vmcnt(8)
	s_waitcnt lgkmcnt(0)
	s_barrier
	s_setprio 1
	s_waitcnt lgkmcnt(0)
	v_mfma_scale_f32_16x16x128_f8f6f4 v[126:129], v[158:161], v[178:181], v[126:129], v191, v191 op_sel_hi:[0,0,0] cbsz:4 blgp:4
	s_nop 0
	v_mfma_scale_f32_16x16x128_f8f6f4 v[126:129], v[154:157], v[182:185], v[126:129], v191, v191 op_sel_hi:[0,0,0] cbsz:4 blgp:4
	v_mfma_scale_f32_16x16x128_f8f6f4 v[122:125], v[150:153], v[178:181], v[122:125], v191, v191 op_sel_hi:[0,0,0] cbsz:4 blgp:4
	s_nop 0
	v_mfma_scale_f32_16x16x128_f8f6f4 v[122:125], v[146:149], v[182:185], v[122:125], v191, v191 op_sel_hi:[0,0,0] cbsz:4 blgp:4
	v_mfma_scale_f32_16x16x128_f8f6f4 v[110:113], v[158:161], v[194:197], v[110:113], v191, v191 op_sel_hi:[0,0,0] cbsz:4 blgp:4
	s_nop 0
	v_mfma_scale_f32_16x16x128_f8f6f4 v[110:113], v[154:157], v[198:201], v[110:113], v191, v191 op_sel_hi:[0,0,0] cbsz:4 blgp:4
	v_mfma_scale_f32_16x16x128_f8f6f4 v[106:109], v[150:153], v[194:197], v[106:109], v191, v191 op_sel_hi:[0,0,0] cbsz:4 blgp:4
	s_nop 0
	v_mfma_scale_f32_16x16x128_f8f6f4 v[106:109], v[146:149], v[198:201], v[106:109], v191, v191 op_sel_hi:[0,0,0] cbsz:4 blgp:4
	v_mfma_scale_f32_16x16x128_f8f6f4 v[94:97], v[158:161], v[202:205], v[94:97], v191, v191 op_sel_hi:[0,0,0] cbsz:4 blgp:4
	s_nop 0
	v_mfma_scale_f32_16x16x128_f8f6f4 v[94:97], v[154:157], v[206:209], v[94:97], v191, v191 op_sel_hi:[0,0,0] cbsz:4 blgp:4
	v_mfma_scale_f32_16x16x128_f8f6f4 v[90:93], v[150:153], v[202:205], v[90:93], v191, v191 op_sel_hi:[0,0,0] cbsz:4 blgp:4
	s_nop 0
	v_mfma_scale_f32_16x16x128_f8f6f4 v[90:93], v[146:149], v[206:209], v[90:93], v191, v191 op_sel_hi:[0,0,0] cbsz:4 blgp:4
	v_mfma_scale_f32_16x16x128_f8f6f4 v[78:81], v[158:161], v[210:213], v[78:81], v191, v191 op_sel_hi:[0,0,0] cbsz:4 blgp:4
	s_nop 0
	v_mfma_scale_f32_16x16x128_f8f6f4 v[78:81], v[154:157], v[214:217], v[78:81], v191, v191 op_sel_hi:[0,0,0] cbsz:4 blgp:4
	v_mfma_scale_f32_16x16x128_f8f6f4 v[74:77], v[150:153], v[210:213], v[74:77], v191, v191 op_sel_hi:[0,0,0] cbsz:4 blgp:4
	s_nop 0
	v_mfma_scale_f32_16x16x128_f8f6f4 v[74:77], v[146:149], v[214:217], v[74:77], v191, v191 op_sel_hi:[0,0,0] cbsz:4 blgp:4
	s_setprio 0
	s_setprio 1
	v_mfma_scale_f32_16x16x128_f8f6f4 v[118:121], v[142:145], v[178:181], v[118:121], v191, v191 op_sel_hi:[0,0,0] cbsz:4 blgp:4
	s_nop 0
	v_mfma_scale_f32_16x16x128_f8f6f4 v[118:121], v[138:141], v[182:185], v[118:121], v191, v191 op_sel_hi:[0,0,0] cbsz:4 blgp:4
	v_mfma_scale_f32_16x16x128_f8f6f4 v[114:117], v[134:137], v[178:181], v[114:117], v191, v191 op_sel_hi:[0,0,0] cbsz:4 blgp:4
	s_nop 0
	v_mfma_scale_f32_16x16x128_f8f6f4 v[114:117], v[130:133], v[182:185], v[114:117], v191, v191 op_sel_hi:[0,0,0] cbsz:4 blgp:4
	v_mfma_scale_f32_16x16x128_f8f6f4 v[102:105], v[142:145], v[194:197], v[102:105], v191, v191 op_sel_hi:[0,0,0] cbsz:4 blgp:4
	s_nop 0
	v_mfma_scale_f32_16x16x128_f8f6f4 v[102:105], v[138:141], v[198:201], v[102:105], v191, v191 op_sel_hi:[0,0,0] cbsz:4 blgp:4
	v_mfma_scale_f32_16x16x128_f8f6f4 v[98:101], v[134:137], v[194:197], v[98:101], v191, v191 op_sel_hi:[0,0,0] cbsz:4 blgp:4
	s_nop 0
	v_mfma_scale_f32_16x16x128_f8f6f4 v[98:101], v[130:133], v[198:201], v[98:101], v191, v191 op_sel_hi:[0,0,0] cbsz:4 blgp:4
	v_mfma_scale_f32_16x16x128_f8f6f4 v[86:89], v[142:145], v[202:205], v[86:89], v191, v191 op_sel_hi:[0,0,0] cbsz:4 blgp:4
	s_nop 0
	v_mfma_scale_f32_16x16x128_f8f6f4 v[86:89], v[138:141], v[206:209], v[86:89], v191, v191 op_sel_hi:[0,0,0] cbsz:4 blgp:4
	v_mfma_scale_f32_16x16x128_f8f6f4 v[82:85], v[134:137], v[202:205], v[82:85], v191, v191 op_sel_hi:[0,0,0] cbsz:4 blgp:4
	s_nop 0
	v_mfma_scale_f32_16x16x128_f8f6f4 v[82:85], v[130:133], v[206:209], v[82:85], v191, v191 op_sel_hi:[0,0,0] cbsz:4 blgp:4
	v_mfma_scale_f32_16x16x128_f8f6f4 v[70:73], v[142:145], v[210:213], v[70:73], v191, v191 op_sel_hi:[0,0,0] cbsz:4 blgp:4
	s_nop 0
	v_mfma_scale_f32_16x16x128_f8f6f4 v[70:73], v[138:141], v[214:217], v[70:73], v191, v191 op_sel_hi:[0,0,0] cbsz:4 blgp:4
	v_mfma_scale_f32_16x16x128_f8f6f4 v[66:69], v[134:137], v[210:213], v[66:69], v191, v191 op_sel_hi:[0,0,0] cbsz:4 blgp:4
	s_nop 0
	v_mfma_scale_f32_16x16x128_f8f6f4 v[66:69], v[130:133], v[214:217], v[66:69], v191, v191 op_sel_hi:[0,0,0] cbsz:4 blgp:4
	s_setprio 0
	s_barrier
; #define PG8_STAGE(bufoff, gbase, voff) do { _Pragma("unroll") for (int _i = 0; _i < 2; ++_i) \
;         __builtin_amdgcn_global_load_lds((const unsigned*)((const char*)(gbase) + (voff)[_i]), (PG8_LAS unsigned*)(lds + (bufoff) + ldsw + _i * 8192), 16, 0, 0); } while (0)
; #define PG8_LDA(dst, b, h) do { _Pragma("unroll") for (int m = 0; m < 4; ++m) _Pragma("unroll") for (int k = 0; k < 2; ++k) dst[m][k] = *(const PG8_LAS bf16x8*)(lds + PG8_SA(b, h) + aoff + m * 2048 + k * 1024); } while (0)
; #define PG8_WAIT_V(n) asm volatile("s_waitcnt vmcnt(" #n ")" ::: "memory")
; #define PG8_WAIT_L(n) asm volatile("s_waitcnt lgkmcnt(" #n ")" ::: "memory")
; #define PG8_BAR __builtin_amdgcn_s_barrier()
; #define PG8_SCHED __builtin_amdgcn_sched_barrier(0)
;     ...
;             PG8_LDA(At, 0, 1); PG8_STAGE(PG8_SB(0, 0), b2, voffB); PG8_STAGE(PG8_SB(0, 1), b2 + hstepB, voffB); PG8_STAGE(PG8_SA(0, 0), a2, voffA);
;             PG8_WAIT_V(8); PG8_WAIT_L(0); PG8_BAR; PG8_MMA(1, 0, At, B0); PG8_MMA(1, 1, At, B1); PG8_BAR; PG8_SCHED;
	s_add_i32 s67, s45, s10
	v_lshl_add_u64 v[178:179], s[80:81], 0, v[164:165]
	s_mov_b32 m0, s67
	ds_read_b128 v[194:197], v190 offset:16384
	ds_read_b128 v[198:201], v190 offset:17408
	ds_read_b128 v[202:205], v190 offset:18432
	ds_read_b128 v[206:209], v190 offset:19456
	ds_read_b128 v[210:213], v190 offset:20480
	ds_read_b128 v[214:217], v190 offset:21504
	ds_read_b128 v[218:221], v190 offset:22528
	ds_read_b128 v[222:225], v190 offset:23552
	global_load_lds_dwordx4 v[178:179], off
	s_add_i32 m0, s67, 0x2000
	s_add_u32 s68, s80, 0x40000
	v_lshl_add_u64 v[180:181], s[80:81], 0, v[168:169]
	s_addc_u32 s69, s81, 0
	s_add_i32 s67, s46, s10
	global_load_lds_dwordx4 v[180:181], off
	v_lshl_add_u64 v[182:183], s[68:69], 0, v[164:165]
	s_mov_b32 m0, s67
	v_lshl_add_u64 v[184:185], s[82:83], 0, v[166:167]
	global_load_lds_dwordx4 v[182:183], off
	v_lshl_add_u64 v[182:183], s[68:69], 0, v[168:169]
	s_add_i32 m0, s67, 0x2000
	s_nop 0
	global_load_lds_dwordx4 v[182:183], off
	v_lshl_add_u64 v[182:183], s[82:83], 0, v[162:163]
	s_mov_b32 m0, s25
	s_nop 0
	global_load_lds_dwordx4 v[182:183], off
	s_mov_b32 m0, s33
	s_nop 0
	global_load_lds_dwordx4 v[184:185], off
	s_waitcnt vmcnt(8)
	s_waitcnt lgkmcnt(0)
	s_barrier
	s_setprio 1
	s_waitcnt lgkmcnt(0)
	v_mfma_scale_f32_16x16x128_f8f6f4 v[62:65], v[158:161], v[194:197], v[62:65], v191, v191 op_sel_hi:[0,0,0] cbsz:4 blgp:4
	s_nop 0
	v_mfma_scale_f32_16x16x128_f8f6f4 v[62:65], v[154:157], v[198:201], v[62:65], v191, v191 op_sel_hi:[0,0,0] cbsz:4 blgp:4
	v_mfma_scale_f32_16x16x128_f8f6f4 v[58:61], v[150:153], v[194:197], v[58:61], v191, v191 op_sel_hi:[0,0,0] cbsz:4 blgp:4
	s_nop 0
	v_mfma_scale_f32_16x16x128_f8f6f4 v[58:61], v[146:149], v[198:201], v[58:61], v191, v191 op_sel_hi:[0,0,0] cbsz:4 blgp:4
	v_mfma_scale_f32_16x16x128_f8f6f4 v[46:49], v[158:161], v[202:205], v[46:49], v191, v191 op_sel_hi:[0,0,0] cbsz:4 blgp:4
	s_nop 0
	v_mfma_scale_f32_16x16x128_f8f6f4 v[46:49], v[154:157], v[206:209], v[46:49], v191, v191 op_sel_hi:[0,0,0] cbsz:4 blgp:4
	v_mfma_scale_f32_16x16x128_f8f6f4 v[42:45], v[150:153], v[202:205], v[42:45], v191, v191 op_sel_hi:[0,0,0] cbsz:4 blgp:4
	s_nop 0
	v_mfma_scale_f32_16x16x128_f8f6f4 v[42:45], v[146:149], v[206:209], v[42:45], v191, v191 op_sel_hi:[0,0,0] cbsz:4 blgp:4
	v_mfma_scale_f32_16x16x128_f8f6f4 v[30:33], v[158:161], v[210:213], v[30:33], v191, v191 op_sel_hi:[0,0,0] cbsz:4 blgp:4
	s_nop 0
	v_mfma_scale_f32_16x16x128_f8f6f4 v[30:33], v[154:157], v[214:217], v[30:33], v191, v191 op_sel_hi:[0,0,0] cbsz:4 blgp:4
	v_mfma_scale_f32_16x16x128_f8f6f4 v[26:29], v[150:153], v[210:213], v[26:29], v191, v191 op_sel_hi:[0,0,0] cbsz:4 blgp:4
	s_nop 0
	v_mfma_scale_f32_16x16x128_f8f6f4 v[26:29], v[146:149], v[214:217], v[26:29], v191, v191 op_sel_hi:[0,0,0] cbsz:4 blgp:4
	v_mfma_scale_f32_16x16x128_f8f6f4 v[14:17], v[158:161], v[218:221], v[14:17], v191, v191 op_sel_hi:[0,0,0] cbsz:4 blgp:4
	s_nop 0
	v_mfma_scale_f32_16x16x128_f8f6f4 v[14:17], v[154:157], v[222:225], v[14:17], v191, v191 op_sel_hi:[0,0,0] cbsz:4 blgp:4
	v_mfma_scale_f32_16x16x128_f8f6f4 v[10:13], v[150:153], v[218:221], v[10:13], v191, v191 op_sel_hi:[0,0,0] cbsz:4 blgp:4
	s_nop 0
	v_mfma_scale_f32_16x16x128_f8f6f4 v[10:13], v[146:149], v[222:225], v[10:13], v191, v191 op_sel_hi:[0,0,0] cbsz:4 blgp:4
	s_setprio 0
	s_setprio 1
	v_mfma_scale_f32_16x16x128_f8f6f4 v[54:57], v[142:145], v[194:197], v[54:57], v191, v191 op_sel_hi:[0,0,0] cbsz:4 blgp:4
	s_nop 0
	v_mfma_scale_f32_16x16x128_f8f6f4 v[54:57], v[138:141], v[198:201], v[54:57], v191, v191 op_sel_hi:[0,0,0] cbsz:4 blgp:4
	v_mfma_scale_f32_16x16x128_f8f6f4 v[50:53], v[134:137], v[194:197], v[50:53], v191, v191 op_sel_hi:[0,0,0] cbsz:4 blgp:4
	s_nop 0
	v_mfma_scale_f32_16x16x128_f8f6f4 v[50:53], v[130:133], v[198:201], v[50:53], v191, v191 op_sel_hi:[0,0,0] cbsz:4 blgp:4
	v_mfma_scale_f32_16x16x128_f8f6f4 v[38:41], v[142:145], v[202:205], v[38:41], v191, v191 op_sel_hi:[0,0,0] cbsz:4 blgp:4
	s_nop 0
	v_mfma_scale_f32_16x16x128_f8f6f4 v[38:41], v[138:141], v[206:209], v[38:41], v191, v191 op_sel_hi:[0,0,0] cbsz:4 blgp:4
	v_mfma_scale_f32_16x16x128_f8f6f4 v[34:37], v[134:137], v[202:205], v[34:37], v191, v191 op_sel_hi:[0,0,0] cbsz:4 blgp:4
	s_nop 0
	v_mfma_scale_f32_16x16x128_f8f6f4 v[34:37], v[130:133], v[206:209], v[34:37], v191, v191 op_sel_hi:[0,0,0] cbsz:4 blgp:4
	v_mfma_scale_f32_16x16x128_f8f6f4 v[22:25], v[142:145], v[210:213], v[22:25], v191, v191 op_sel_hi:[0,0,0] cbsz:4 blgp:4
	s_nop 0
	v_mfma_scale_f32_16x16x128_f8f6f4 v[22:25], v[138:141], v[214:217], v[22:25], v191, v191 op_sel_hi:[0,0,0] cbsz:4 blgp:4
	v_mfma_scale_f32_16x16x128_f8f6f4 v[18:21], v[134:137], v[210:213], v[18:21], v191, v191 op_sel_hi:[0,0,0] cbsz:4 blgp:4
	s_nop 0
	v_mfma_scale_f32_16x16x128_f8f6f4 v[18:21], v[130:133], v[214:217], v[18:21], v191, v191 op_sel_hi:[0,0,0] cbsz:4 blgp:4
	v_mfma_scale_f32_16x16x128_f8f6f4 v[6:9], v[142:145], v[218:221], v[6:9], v191, v191 op_sel_hi:[0,0,0] cbsz:4 blgp:4
	s_nop 0
	v_mfma_scale_f32_16x16x128_f8f6f4 v[6:9], v[138:141], v[222:225], v[6:9], v191, v191 op_sel_hi:[0,0,0] cbsz:4 blgp:4
	v_mfma_scale_f32_16x16x128_f8f6f4 v[2:5], v[134:137], v[218:221], v[2:5], v191, v191 op_sel_hi:[0,0,0] cbsz:4 blgp:4
	s_nop 0
	v_mfma_scale_f32_16x16x128_f8f6f4 v[2:5], v[130:133], v[222:225], v[2:5], v191, v191 op_sel_hi:[0,0,0] cbsz:4 blgp:4
	s_setprio 0
	s_barrier
; #define PG8_STAGE(bufoff, gbase, voff) do { _Pragma("unroll") for (int _i = 0; _i < 2; ++_i) \
;         __builtin_amdgcn_global_load_lds((const unsigned*)((const char*)(gbase) + (voff)[_i]), (PG8_LAS unsigned*)(lds + (bufoff) + ldsw + _i * 8192), 16, 0, 0); } while (0)
; #define PG8_LDA(dst, b, h) do { _Pragma("unroll") for (int m = 0; m < 4; ++m) _Pragma("unroll") for (int k = 0; k < 2; ++k) dst[m][k] = *(const PG8_LAS bf16x8*)(lds + PG8_SA(b, h) + aoff + m * 2048 + k * 1024); } while (0)
; #define PG8_LDB(dst, b, h) do { _Pragma("unroll") for (int n = 0; n < 2; ++n) _Pragma("unroll") for (int k = 0; k < 2; ++k) dst[n][k] = *(const PG8_LAS bf16x8*)(lds + PG8_SB(b, h) + boff + n * 2048 + k * 1024); } while (0)
; #define PG8_WAIT_V(n) asm volatile("s_waitcnt vmcnt(" #n ")" ::: "memory")
; #define PG8_WAIT_L(n) asm volatile("s_waitcnt lgkmcnt(" #n ")" ::: "memory")
; #define PG8_BAR __builtin_amdgcn_s_barrier()
; #define PG8_SCHED __builtin_amdgcn_sched_barrier(0)
;     ...
;             PG8_LDB(B0, 1, 0); PG8_LDB(B1, 1, 1); PG8_SCHED; PG8_LDA(At, 1, 0); PG8_STAGE(PG8_SA(0, 1), a2 + hstepA, voffA);
;             PG8_WAIT_V(8); PG8_WAIT_L(0); PG8_BAR; PG8_MMA(0, 0, At, B0); PG8_MMA(0, 1, At, B1); PG8_BAR; PG8_SCHED;
	s_add_i32 s67, 0, 0x18000
	s_add_i32 s70, 0, 0x1c000
	v_add_u32_e32 v142, s67, v192
	v_add_u32_e32 v158, s70, v192
	ds_read_b128 v[130:133], v142
	ds_read_b128 v[134:137], v142 offset:1024
	ds_read_b128 v[138:141], v142 offset:2048
	ds_read_b128 v[142:145], v142 offset:3072
	ds_read_b128 v[146:149], v158
	ds_read_b128 v[150:153], v158 offset:1024
	ds_read_b128 v[154:157], v158 offset:2048
	ds_read_b128 v[158:161], v158 offset:3072
	s_add_u32 s68, s82, 0x40000
	s_addc_u32 s69, s83, 0
	s_mov_b32 m0, s34
	v_lshl_add_u64 v[226:227], s[68:69], 0, v[162:163]
	ds_read_b128 v[194:197], v190 offset:32768
	ds_read_b128 v[198:201], v190 offset:33792
	ds_read_b128 v[202:205], v190 offset:34816
	ds_read_b128 v[206:209], v190 offset:35840
	ds_read_b128 v[210:213], v190 offset:36864
	ds_read_b128 v[214:217], v190 offset:37888
	ds_read_b128 v[218:221], v190 offset:38912
	ds_read_b128 v[222:225], v190 offset:39936
	global_load_lds_dwordx4 v[226:227], off
	v_lshl_add_u64 v[226:227], s[68:69], 0, v[166:167]
	s_mov_b32 m0, s35
	s_nop 0
	global_load_lds_dwordx4 v[226:227], off
	s_waitcnt vmcnt(8)
	s_waitcnt lgkmcnt(0)
	s_barrier
	s_setprio 1
	s_waitcnt lgkmcnt(0)
	v_mfma_scale_f32_16x16x128_f8f6f4 v[126:129], v[130:133], v[194:197], v[126:129], v191, v191 op_sel_hi:[0,0,0] cbsz:4 blgp:4
	s_nop 0
	v_mfma_scale_f32_16x16x128_f8f6f4 v[126:129], v[134:137], v[198:201], v[126:129], v191, v191 op_sel_hi:[0,0,0] cbsz:4 blgp:4
	v_mfma_scale_f32_16x16x128_f8f6f4 v[122:125], v[138:141], v[194:197], v[122:125], v191, v191 op_sel_hi:[0,0,0] cbsz:4 blgp:4
	s_nop 0
	v_mfma_scale_f32_16x16x128_f8f6f4 v[122:125], v[142:145], v[198:201], v[122:125], v191, v191 op_sel_hi:[0,0,0] cbsz:4 blgp:4
	v_mfma_scale_f32_16x16x128_f8f6f4 v[110:113], v[130:133], v[202:205], v[110:113], v191, v191 op_sel_hi:[0,0,0] cbsz:4 blgp:4
	s_nop 0
	v_mfma_scale_f32_16x16x128_f8f6f4 v[110:113], v[134:137], v[206:209], v[110:113], v191, v191 op_sel_hi:[0,0,0] cbsz:4 blgp:4
	v_mfma_scale_f32_16x16x128_f8f6f4 v[106:109], v[138:141], v[202:205], v[106:109], v191, v191 op_sel_hi:[0,0,0] cbsz:4 blgp:4
	s_nop 0
	v_mfma_scale_f32_16x16x128_f8f6f4 v[106:109], v[142:145], v[206:209], v[106:109], v191, v191 op_sel_hi:[0,0,0] cbsz:4 blgp:4
	v_mfma_scale_f32_16x16x128_f8f6f4 v[94:97], v[130:133], v[210:213], v[94:97], v191, v191 op_sel_hi:[0,0,0] cbsz:4 blgp:4
	s_nop 0
	v_mfma_scale_f32_16x16x128_f8f6f4 v[94:97], v[134:137], v[214:217], v[94:97], v191, v191 op_sel_hi:[0,0,0] cbsz:4 blgp:4
	v_mfma_scale_f32_16x16x128_f8f6f4 v[90:93], v[138:141], v[210:213], v[90:93], v191, v191 op_sel_hi:[0,0,0] cbsz:4 blgp:4
	s_nop 0
	v_mfma_scale_f32_16x16x128_f8f6f4 v[90:93], v[142:145], v[214:217], v[90:93], v191, v191 op_sel_hi:[0,0,0] cbsz:4 blgp:4
	v_mfma_scale_f32_16x16x128_f8f6f4 v[78:81], v[130:133], v[218:221], v[78:81], v191, v191 op_sel_hi:[0,0,0] cbsz:4 blgp:4
	s_nop 0
	v_mfma_scale_f32_16x16x128_f8f6f4 v[78:81], v[134:137], v[222:225], v[78:81], v191, v191 op_sel_hi:[0,0,0] cbsz:4 blgp:4
	v_mfma_scale_f32_16x16x128_f8f6f4 v[74:77], v[138:141], v[218:221], v[74:77], v191, v191 op_sel_hi:[0,0,0] cbsz:4 blgp:4
	s_nop 0
	v_mfma_scale_f32_16x16x128_f8f6f4 v[74:77], v[142:145], v[222:225], v[74:77], v191, v191 op_sel_hi:[0,0,0] cbsz:4 blgp:4
	s_setprio 0
	s_setprio 1
	v_mfma_scale_f32_16x16x128_f8f6f4 v[118:121], v[146:149], v[194:197], v[118:121], v191, v191 op_sel_hi:[0,0,0] cbsz:4 blgp:4
	s_nop 0
	v_mfma_scale_f32_16x16x128_f8f6f4 v[118:121], v[150:153], v[198:201], v[118:121], v191, v191 op_sel_hi:[0,0,0] cbsz:4 blgp:4
	v_mfma_scale_f32_16x16x128_f8f6f4 v[114:117], v[154:157], v[194:197], v[114:117], v191, v191 op_sel_hi:[0,0,0] cbsz:4 blgp:4
	s_nop 0
	v_mfma_scale_f32_16x16x128_f8f6f4 v[114:117], v[158:161], v[198:201], v[114:117], v191, v191 op_sel_hi:[0,0,0] cbsz:4 blgp:4
	v_mfma_scale_f32_16x16x128_f8f6f4 v[102:105], v[146:149], v[202:205], v[102:105], v191, v191 op_sel_hi:[0,0,0] cbsz:4 blgp:4
	s_nop 0
	v_mfma_scale_f32_16x16x128_f8f6f4 v[102:105], v[150:153], v[206:209], v[102:105], v191, v191 op_sel_hi:[0,0,0] cbsz:4 blgp:4
	v_mfma_scale_f32_16x16x128_f8f6f4 v[98:101], v[154:157], v[202:205], v[98:101], v191, v191 op_sel_hi:[0,0,0] cbsz:4 blgp:4
	s_nop 0
	v_mfma_scale_f32_16x16x128_f8f6f4 v[98:101], v[158:161], v[206:209], v[98:101], v191, v191 op_sel_hi:[0,0,0] cbsz:4 blgp:4
	v_mfma_scale_f32_16x16x128_f8f6f4 v[86:89], v[146:149], v[210:213], v[86:89], v191, v191 op_sel_hi:[0,0,0] cbsz:4 blgp:4
	s_nop 0
	v_mfma_scale_f32_16x16x128_f8f6f4 v[86:89], v[150:153], v[214:217], v[86:89], v191, v191 op_sel_hi:[0,0,0] cbsz:4 blgp:4
	v_mfma_scale_f32_16x16x128_f8f6f4 v[82:85], v[154:157], v[210:213], v[82:85], v191, v191 op_sel_hi:[0,0,0] cbsz:4 blgp:4
	s_nop 0
	v_mfma_scale_f32_16x16x128_f8f6f4 v[82:85], v[158:161], v[214:217], v[82:85], v191, v191 op_sel_hi:[0,0,0] cbsz:4 blgp:4
	v_mfma_scale_f32_16x16x128_f8f6f4 v[70:73], v[146:149], v[218:221], v[70:73], v191, v191 op_sel_hi:[0,0,0] cbsz:4 blgp:4
	s_nop 0
	v_mfma_scale_f32_16x16x128_f8f6f4 v[70:73], v[150:153], v[222:225], v[70:73], v191, v191 op_sel_hi:[0,0,0] cbsz:4 blgp:4
	v_mfma_scale_f32_16x16x128_f8f6f4 v[66:69], v[154:157], v[218:221], v[66:69], v191, v191 op_sel_hi:[0,0,0] cbsz:4 blgp:4
	s_nop 0
	v_mfma_scale_f32_16x16x128_f8f6f4 v[66:69], v[158:161], v[222:225], v[66:69], v191, v191 op_sel_hi:[0,0,0] cbsz:4 blgp:4
	s_setprio 0
	s_barrier
; #define PG8_STAGE(bufoff, gbase, voff) do { _Pragma("unroll") for (int _i = 0; _i < 2; ++_i) \
;         __builtin_amdgcn_global_load_lds((const unsigned*)((const char*)(gbase) + (voff)[_i]), (PG8_LAS unsigned*)(lds + (bufoff) + ldsw + _i * 8192), 16, 0, 0); } while (0)
; #define PG8_LDA(dst, b, h) do { _Pragma("unroll") for (int m = 0; m < 4; ++m) _Pragma("unroll") for (int k = 0; k < 2; ++k) dst[m][k] = *(const PG8_LAS bf16x8*)(lds + PG8_SA(b, h) + aoff + m * 2048 + k * 1024); } while (0)
; #define PG8_WAIT_V(n) asm volatile("s_waitcnt vmcnt(" #n ")" ::: "memory")
; #define PG8_BAR __builtin_amdgcn_s_barrier()
;     ...
;         for (int t = 0; t < nt; t += 2) {
;             const bool last = (t == nt - 2);
;             const char* a1 = cA + (size_t)(t + 1) * kstep;
;             const char* a2 = last ? nA : cA + (size_t)(t + 2) * kstep; const char* b2 = last ? nB : cB + (size_t)(t + 2) * kstep;
;             const char* a3 = a2 + kstep; const char* b3 = b2 + kstep;
;             if (last && has_next) S.a_ready(nxt);
;             if constexpr (Epi::MIDK > 0) { if (t == Epi::MIDK) {
;                 if constexpr (FP8) asm volatile("s_nop 15\n\ts_nop 15" ::: "memory");
;                 E.mid(acc, cur, wr, wc, fr, fq);
;                 if constexpr (FP8) asm volatile("s_nop 7" ::: "memory"); } }
;             if constexpr (SP2) {
;             PG8_LDB(B0, 0, 0); PG8_LDB(B1, 0, 1); PG8_SCHED; PG8_LDA(At, 0, 0); PG8_STAGE(PG8_SA(1, 1), a1 + hstepA, voffA);
;             PG8_WAIT_V(8); PG8_WAIT_L(0); PG8_BAR; PG8_MMA(0, 0, At, B0); PG8_MMA(0, 1, At, B1); PG8_BAR; PG8_SCHED;
;             PG8_LDA(At, 0, 1); PG8_STAGE(PG8_SB(0, 0), b2, voffB); PG8_STAGE(PG8_SB(0, 1), b2 + hstepB, voffB); PG8_STAGE(PG8_SA(0, 0), a2, voffA);
;             PG8_WAIT_V(8); PG8_WAIT_L(0); PG8_BAR; PG8_MMA(1, 0, At, B0); PG8_MMA(1, 1, At, B1); PG8_BAR; PG8_SCHED;
;             PG8_LDB(B0, 1, 0); PG8_LDB(B1, 1, 1); PG8_SCHED; PG8_LDA(At, 1, 0); PG8_STAGE(PG8_SA(0, 1), a2 + hstepA, voffA);
;             PG8_WAIT_V(8); PG8_WAIT_L(0); PG8_BAR; PG8_MMA(0, 0, At, B0); PG8_MMA(0, 1, At, B1); PG8_BAR; PG8_SCHED;
;             PG8_LDA(At, 1, 1); PG8_STAGE(PG8_SB(1, 0), b3, voffB); PG8_STAGE(PG8_SB(1, 1), b3 + hstepB, voffB); PG8_STAGE(PG8_SA(1, 0), a3, voffA);
;             PG8_WAIT_V(8); PG8_WAIT_L(0); PG8_BAR; PG8_MMA(1, 0, At, B0); PG8_MMA(1, 1, At, B1); PG8_BAR; PG8_SCHED;
	s_add_i32 s67, s67, s10
	v_lshl_add_u64 v[178:179], v[178:179], 0, s[20:21]
	s_mov_b32 m0, s67
	ds_read_b128 v[194:197], v190 offset:49152
	ds_read_b128 v[198:201], v190 offset:50176
	ds_read_b128 v[202:205], v190 offset:51200
	ds_read_b128 v[206:209], v190 offset:52224
	ds_read_b128 v[210:213], v190 offset:53248
	ds_read_b128 v[214:217], v190 offset:54272
	ds_read_b128 v[218:221], v190 offset:55296
	ds_read_b128 v[222:225], v190 offset:56320
	global_load_lds_dwordx4 v[178:179], off
	s_add_i32 m0, s67, 0x2000
	s_add_u32 s68, s80, 0x40080
	v_lshl_add_u64 v[178:179], v[180:181], 0, s[20:21]
	s_addc_u32 s69, s81, 0
	s_add_i32 s67, s70, s10
	global_load_lds_dwordx4 v[178:179], off
	v_lshl_add_u64 v[178:179], s[68:69], 0, v[164:165]
	s_mov_b32 m0, s67
	s_nop 0
	global_load_lds_dwordx4 v[178:179], off
	v_lshl_add_u64 v[178:179], s[68:69], 0, v[168:169]
	s_add_i32 m0, s67, 0x2000
	s_nop 0
	global_load_lds_dwordx4 v[178:179], off
	v_lshl_add_u64 v[178:179], v[182:183], 0, s[20:21]
	s_mov_b32 m0, s43
	s_nop 0
	global_load_lds_dwordx4 v[178:179], off
	v_lshl_add_u64 v[178:179], v[184:185], 0, s[20:21]
	s_mov_b32 m0, s44
	s_nop 0
	global_load_lds_dwordx4 v[178:179], off
	s_waitcnt vmcnt(8)
	s_waitcnt lgkmcnt(0)
	s_barrier
	s_setprio 1
	s_waitcnt lgkmcnt(0)
	v_mfma_scale_f32_16x16x128_f8f6f4 v[62:65], v[130:133], v[194:197], v[62:65], v191, v191 op_sel_hi:[0,0,0] cbsz:4 blgp:4
	s_nop 0
	v_mfma_scale_f32_16x16x128_f8f6f4 v[62:65], v[134:137], v[198:201], v[62:65], v191, v191 op_sel_hi:[0,0,0] cbsz:4 blgp:4
	v_mfma_scale_f32_16x16x128_f8f6f4 v[58:61], v[138:141], v[194:197], v[58:61], v191, v191 op_sel_hi:[0,0,0] cbsz:4 blgp:4
	s_nop 0
	v_mfma_scale_f32_16x16x128_f8f6f4 v[58:61], v[142:145], v[198:201], v[58:61], v191, v191 op_sel_hi:[0,0,0] cbsz:4 blgp:4
	v_mfma_scale_f32_16x16x128_f8f6f4 v[46:49], v[130:133], v[202:205], v[46:49], v191, v191 op_sel_hi:[0,0,0] cbsz:4 blgp:4
	s_nop 0
	v_mfma_scale_f32_16x16x128_f8f6f4 v[46:49], v[134:137], v[206:209], v[46:49], v191, v191 op_sel_hi:[0,0,0] cbsz:4 blgp:4
	v_mfma_scale_f32_16x16x128_f8f6f4 v[42:45], v[138:141], v[202:205], v[42:45], v191, v191 op_sel_hi:[0,0,0] cbsz:4 blgp:4
	s_nop 0
	v_mfma_scale_f32_16x16x128_f8f6f4 v[42:45], v[142:145], v[206:209], v[42:45], v191, v191 op_sel_hi:[0,0,0] cbsz:4 blgp:4
	v_mfma_scale_f32_16x16x128_f8f6f4 v[30:33], v[130:133], v[210:213], v[30:33], v191, v191 op_sel_hi:[0,0,0] cbsz:4 blgp:4
	s_nop 0
	v_mfma_scale_f32_16x16x128_f8f6f4 v[30:33], v[134:137], v[214:217], v[30:33], v191, v191 op_sel_hi:[0,0,0] cbsz:4 blgp:4
	v_mfma_scale_f32_16x16x128_f8f6f4 v[26:29], v[138:141], v[210:213], v[26:29], v191, v191 op_sel_hi:[0,0,0] cbsz:4 blgp:4
	s_nop 0
	v_mfma_scale_f32_16x16x128_f8f6f4 v[26:29], v[142:145], v[214:217], v[26:29], v191, v191 op_sel_hi:[0,0,0] cbsz:4 blgp:4
	v_mfma_scale_f32_16x16x128_f8f6f4 v[14:17], v[130:133], v[218:221], v[14:17], v191, v191 op_sel_hi:[0,0,0] cbsz:4 blgp:4
	s_nop 0
	v_mfma_scale_f32_16x16x128_f8f6f4 v[14:17], v[134:137], v[222:225], v[14:17], v191, v191 op_sel_hi:[0,0,0] cbsz:4 blgp:4
	v_mfma_scale_f32_16x16x128_f8f6f4 v[10:13], v[138:141], v[218:221], v[10:13], v191, v191 op_sel_hi:[0,0,0] cbsz:4 blgp:4
	s_nop 0
	v_mfma_scale_f32_16x16x128_f8f6f4 v[10:13], v[142:145], v[222:225], v[10:13], v191, v191 op_sel_hi:[0,0,0] cbsz:4 blgp:4
	s_setprio 0
	s_setprio 1
	v_mfma_scale_f32_16x16x128_f8f6f4 v[54:57], v[146:149], v[194:197], v[54:57], v191, v191 op_sel_hi:[0,0,0] cbsz:4 blgp:4
	s_nop 0
	v_mfma_scale_f32_16x16x128_f8f6f4 v[54:57], v[150:153], v[198:201], v[54:57], v191, v191 op_sel_hi:[0,0,0] cbsz:4 blgp:4
	v_mfma_scale_f32_16x16x128_f8f6f4 v[50:53], v[154:157], v[194:197], v[50:53], v191, v191 op_sel_hi:[0,0,0] cbsz:4 blgp:4
	s_nop 0
	v_mfma_scale_f32_16x16x128_f8f6f4 v[50:53], v[158:161], v[198:201], v[50:53], v191, v191 op_sel_hi:[0,0,0] cbsz:4 blgp:4
	v_mfma_scale_f32_16x16x128_f8f6f4 v[38:41], v[146:149], v[202:205], v[38:41], v191, v191 op_sel_hi:[0,0,0] cbsz:4 blgp:4
	s_nop 0
	v_mfma_scale_f32_16x16x128_f8f6f4 v[38:41], v[150:153], v[206:209], v[38:41], v191, v191 op_sel_hi:[0,0,0] cbsz:4 blgp:4
	v_mfma_scale_f32_16x16x128_f8f6f4 v[34:37], v[154:157], v[202:205], v[34:37], v191, v191 op_sel_hi:[0,0,0] cbsz:4 blgp:4
	s_nop 0
	v_mfma_scale_f32_16x16x128_f8f6f4 v[34:37], v[158:161], v[206:209], v[34:37], v191, v191 op_sel_hi:[0,0,0] cbsz:4 blgp:4
	v_mfma_scale_f32_16x16x128_f8f6f4 v[22:25], v[146:149], v[210:213], v[22:25], v191, v191 op_sel_hi:[0,0,0] cbsz:4 blgp:4
	s_nop 0
	v_mfma_scale_f32_16x16x128_f8f6f4 v[22:25], v[150:153], v[214:217], v[22:25], v191, v191 op_sel_hi:[0,0,0] cbsz:4 blgp:4
	v_mfma_scale_f32_16x16x128_f8f6f4 v[18:21], v[154:157], v[210:213], v[18:21], v191, v191 op_sel_hi:[0,0,0] cbsz:4 blgp:4
	s_nop 0
	v_mfma_scale_f32_16x16x128_f8f6f4 v[18:21], v[158:161], v[214:217], v[18:21], v191, v191 op_sel_hi:[0,0,0] cbsz:4 blgp:4
	v_mfma_scale_f32_16x16x128_f8f6f4 v[6:9], v[146:149], v[218:221], v[6:9], v191, v191 op_sel_hi:[0,0,0] cbsz:4 blgp:4
	s_nop 0
	v_mfma_scale_f32_16x16x128_f8f6f4 v[6:9], v[150:153], v[222:225], v[6:9], v191, v191 op_sel_hi:[0,0,0] cbsz:4 blgp:4
	v_mfma_scale_f32_16x16x128_f8f6f4 v[2:5], v[154:157], v[218:221], v[2:5], v191, v191 op_sel_hi:[0,0,0] cbsz:4 blgp:4
	s_nop 0
	v_mfma_scale_f32_16x16x128_f8f6f4 v[2:5], v[158:161], v[222:225], v[2:5], v191, v191 op_sel_hi:[0,0,0] cbsz:4 blgp:4
	s_setprio 0
	s_add_i32 s66, s66, 2
	s_add_u32 s78, s78, 0x100
	s_addc_u32 s79, s79, 0
	s_add_u32 s62, s62, 0x100
	s_addc_u32 s63, s63, 0
	s_cmp_gt_u32 s66, 13
	s_barrier
	s_cbranch_scc0 .LBB0_289
	s_and_b64 vcc, exec, s[22:23]
	s_cbranch_vccz .LBB0_292
	s_barrier

; #define PG8_STAGE(bufoff, gbase, voff) do { _Pragma("unroll") for (int _i = 0; _i < 2; ++_i) \
;         __builtin_amdgcn_global_load_lds((const unsigned*)((const char*)(gbase) + (voff)[_i]), (PG8_LAS unsigned*)(lds + (bufoff) + ldsw + _i * 8192), 16, 0, 0); } while (0)
; #define PG8_LDA(dst, b, h) do { _Pragma("unroll") for (int m = 0; m < 4; ++m) _Pragma("unroll") for (int k = 0; k < 2; ++k) dst[m][k] = *(const PG8_LAS bf16x8*)(lds + PG8_SA(b, h) + aoff + m * 2048 + k * 1024); } while (0)
; #define PG8_LDB(dst, b, h) do { _Pragma("unroll") for (int n = 0; n < 2; ++n) _Pragma("unroll") for (int k = 0; k < 2; ++k) dst[n][k] = *(const PG8_LAS bf16x8*)(lds + PG8_SB(b, h) + boff + n * 2048 + k * 1024); } while (0)
; #define PG8_WAIT_V(n) asm volatile("s_waitcnt vmcnt(" #n ")" ::: "memory")
; #define PG8_WAIT_L(n) asm volatile("s_waitcnt lgkmcnt(" #n ")" ::: "memory")
; #define PG8_BAR __builtin_amdgcn_s_barrier()
; #define PG8_SCHED __builtin_amdgcn_sched_barrier(0)
;     ...
;             const bool last = (t == nt - 2);
;             const char* a1 = cA + (size_t)(t + 1) * kstep;
;             const char* a2 = last ? nA : cA + (size_t)(t + 2) * kstep; const char* b2 = last ? nB : cB + (size_t)(t + 2) * kstep;
;             const char* a3 = a2 + kstep; const char* b3 = b2 + kstep;
;             if (last && has_next) S.a_ready(nxt);
;             if constexpr (Epi::MIDK > 0) { if (t == Epi::MIDK) {
;                 if constexpr (FP8) asm volatile("s_nop 15\n\ts_nop 15" ::: "memory");
;                 E.mid(acc, cur, wr, wc, fr, fq);
;                 if constexpr (FP8) asm volatile("s_nop 7" ::: "memory"); } }
;             if constexpr (SP2) {
;             PG8_LDB(B0, 0, 0); PG8_LDB(B1, 0, 1); PG8_SCHED; PG8_LDA(At, 0, 0); PG8_STAGE(PG8_SA(1, 1), a1 + hstepA, voffA);
;             PG8_WAIT_V(8); PG8_WAIT_L(0); PG8_BAR; PG8_MMA(0, 0, At, B0); PG8_MMA(0, 1, At, B1); PG8_BAR; PG8_SCHED;
;             PG8_LDA(At, 0, 1); PG8_STAGE(PG8_SB(0, 0), b2, voffB); PG8_STAGE(PG8_SB(0, 1), b2 + hstepB, voffB); PG8_STAGE(PG8_SA(0, 0), a2, voffA);
;             PG8_WAIT_V(8); PG8_WAIT_L(0); PG8_BAR; PG8_MMA(1, 0, At, B0); PG8_MMA(1, 1, At, B1); PG8_BAR; PG8_SCHED;
.LBB0_623:
	v_add_u32_e32 v14, s46, v198
	v_add_u32_e32 v30, s47, v198
	s_add_u32 s0, s24, s26
	ds_read_b128 v[2:5], v14
	ds_read_b128 v[6:9], v14 offset:1024
	ds_read_b128 v[10:13], v14 offset:2048
	ds_read_b128 v[14:17], v14 offset:3072
	ds_read_b128 v[18:21], v30
	ds_read_b128 v[22:25], v30 offset:1024
	ds_read_b128 v[26:29], v30 offset:2048
	ds_read_b128 v[30:33], v30 offset:3072
	s_addc_u32 s1, s25, s27
	s_add_u32 s0, s0, 0x100
	s_addc_u32 s1, s1, 0
	s_add_u32 s28, s68, s26
	s_addc_u32 s29, s69, s27
	s_cmpk_eq_i32 s26, 0x900
	s_cselect_b32 s31, s7, s1
	s_cselect_b32 s30, s6, s0
	s_cselect_b32 s29, s23, s29
	s_cselect_b32 s28, s22, s28
	v_lshl_add_u64 v[36:37], v[186:187], 0, s[26:27]
	s_add_i32 m0, s35, 0xc000
	ds_read_b128 v[204:207], v201
	ds_read_b128 v[208:211], v201 offset:1024
	ds_read_b128 v[212:215], v201 offset:2048
	ds_read_b128 v[216:219], v201 offset:3072
	ds_read_b128 v[220:223], v201 offset:4096
	ds_read_b128 v[224:227], v201 offset:5120
	ds_read_b128 v[228:231], v201 offset:6144
	ds_read_b128 v[232:235], v201 offset:7168
	global_load_lds_dwordx4 v[36:37], off
	v_lshl_add_u64 v[36:37], v[188:189], 0, s[26:27]
	s_add_i32 m0, s35, 0xe000
	s_nop 0
	global_load_lds_dwordx4 v[36:37], off
	s_waitcnt vmcnt(8)
	s_waitcnt lgkmcnt(0)
	s_barrier
	s_setprio 1
	s_waitcnt lgkmcnt(0)
	v_mfma_scale_f32_16x16x128_f8f6f4 v[162:165], v[2:9], v[204:211], v[162:165], v202, v202 op_sel_hi:[0,0,0]
	v_mfma_scale_f32_16x16x128_f8f6f4 v[158:161], v[10:17], v[204:211], v[158:161], v202, v202 op_sel_hi:[0,0,0]
	v_mfma_scale_f32_16x16x128_f8f6f4 v[154:157], v[2:9], v[212:219], v[154:157], v202, v202 op_sel_hi:[0,0,0]
	v_mfma_scale_f32_16x16x128_f8f6f4 v[150:153], v[10:17], v[212:219], v[150:153], v202, v202 op_sel_hi:[0,0,0]
	v_mfma_scale_f32_16x16x128_f8f6f4 v[146:149], v[2:9], v[220:227], v[146:149], v202, v202 op_sel_hi:[0,0,0]
	v_mfma_scale_f32_16x16x128_f8f6f4 v[142:145], v[10:17], v[220:227], v[142:145], v202, v202 op_sel_hi:[0,0,0]
	v_mfma_scale_f32_16x16x128_f8f6f4 v[138:141], v[2:9], v[228:235], v[138:141], v202, v202 op_sel_hi:[0,0,0]
	v_mfma_scale_f32_16x16x128_f8f6f4 v[134:137], v[10:17], v[228:235], v[134:137], v202, v202 op_sel_hi:[0,0,0]
	s_setprio 0
	s_setprio 1
	v_mfma_scale_f32_16x16x128_f8f6f4 v[98:101], v[18:25], v[204:211], v[98:101], v202, v202 op_sel_hi:[0,0,0]
	v_mfma_scale_f32_16x16x128_f8f6f4 v[94:97], v[26:33], v[204:211], v[94:97], v202, v202 op_sel_hi:[0,0,0]
	v_mfma_scale_f32_16x16x128_f8f6f4 v[90:93], v[18:25], v[212:219], v[90:93], v202, v202 op_sel_hi:[0,0,0]
	v_mfma_scale_f32_16x16x128_f8f6f4 v[86:89], v[26:33], v[212:219], v[86:89], v202, v202 op_sel_hi:[0,0,0]
	v_mfma_scale_f32_16x16x128_f8f6f4 v[82:85], v[18:25], v[220:227], v[82:85], v202, v202 op_sel_hi:[0,0,0]
	v_mfma_scale_f32_16x16x128_f8f6f4 v[78:81], v[26:33], v[220:227], v[78:81], v202, v202 op_sel_hi:[0,0,0]
	v_mfma_scale_f32_16x16x128_f8f6f4 v[74:77], v[18:25], v[228:235], v[74:77], v202, v202 op_sel_hi:[0,0,0]
	v_mfma_scale_f32_16x16x128_f8f6f4 v[70:73], v[26:33], v[228:235], v[70:73], v202, v202 op_sel_hi:[0,0,0]
	s_setprio 0
	s_barrier
	s_add_i32 s0, s46, s10
	v_lshl_add_u64 v[36:37], s[28:29], 0, v[168:169]
	s_mov_b32 m0, s0
	ds_read_b128 v[204:207], v201 offset:16384
	ds_read_b128 v[208:211], v201 offset:17408
	ds_read_b128 v[212:215], v201 offset:18432
	ds_read_b128 v[216:219], v201 offset:19456
	ds_read_b128 v[220:223], v201 offset:20480
	ds_read_b128 v[224:227], v201 offset:21504
	ds_read_b128 v[228:231], v201 offset:22528
	ds_read_b128 v[232:235], v201 offset:23552
	global_load_lds_dwordx4 v[36:37], off
	s_add_i32 m0, s0, 0x2000
	s_add_u32 s0, s28, 0x50000
	v_lshl_add_u64 v[190:191], s[28:29], 0, v[172:173]
	s_addc_u32 s1, s29, 0
	s_add_i32 s71, s47, s10
	global_load_lds_dwordx4 v[190:191], off
	v_lshl_add_u64 v[192:193], s[0:1], 0, v[168:169]
	s_mov_b32 m0, s71
	v_lshl_add_u64 v[194:195], s[30:31], 0, v[170:171]
	global_load_lds_dwordx4 v[192:193], off
	v_lshl_add_u64 v[192:193], s[0:1], 0, v[172:173]
	s_add_i32 m0, s71, 0x2000
	s_nop 0
	global_load_lds_dwordx4 v[192:193], off
	v_lshl_add_u64 v[192:193], s[30:31], 0, v[166:167]
	s_mov_b32 m0, s35
	s_nop 0
	global_load_lds_dwordx4 v[192:193], off
	s_mov_b32 m0, s36
	s_nop 0
	global_load_lds_dwordx4 v[194:195], off
	s_waitcnt vmcnt(8)
	s_waitcnt lgkmcnt(0)
	s_barrier
	s_setprio 1
	s_waitcnt lgkmcnt(0)
	v_mfma_scale_f32_16x16x128_f8f6f4 v[130:133], v[2:9], v[204:211], v[130:133], v202, v202 op_sel_hi:[0,0,0]
	v_mfma_scale_f32_16x16x128_f8f6f4 v[126:129], v[10:17], v[204:211], v[126:129], v202, v202 op_sel_hi:[0,0,0]
	v_mfma_scale_f32_16x16x128_f8f6f4 v[122:125], v[2:9], v[212:219], v[122:125], v202, v202 op_sel_hi:[0,0,0]
	v_mfma_scale_f32_16x16x128_f8f6f4 v[118:121], v[10:17], v[212:219], v[118:121], v202, v202 op_sel_hi:[0,0,0]
	v_mfma_scale_f32_16x16x128_f8f6f4 v[114:117], v[2:9], v[220:227], v[114:117], v202, v202 op_sel_hi:[0,0,0]
	v_mfma_scale_f32_16x16x128_f8f6f4 v[110:113], v[10:17], v[220:227], v[110:113], v202, v202 op_sel_hi:[0,0,0]
	v_mfma_scale_f32_16x16x128_f8f6f4 v[106:109], v[2:9], v[228:235], v[106:109], v202, v202 op_sel_hi:[0,0,0]
	v_mfma_scale_f32_16x16x128_f8f6f4 v[102:105], v[10:17], v[228:235], v[102:105], v202, v202 op_sel_hi:[0,0,0]
	s_setprio 0
	s_setprio 1
	v_mfma_scale_f32_16x16x128_f8f6f4 v[66:69], v[18:25], v[204:211], v[66:69], v202, v202 op_sel_hi:[0,0,0]
	v_mfma_scale_f32_16x16x128_f8f6f4 v[62:65], v[26:33], v[204:211], v[62:65], v202, v202 op_sel_hi:[0,0,0]
	v_mfma_scale_f32_16x16x128_f8f6f4 v[58:61], v[18:25], v[212:219], v[58:61], v202, v202 op_sel_hi:[0,0,0]
	v_mfma_scale_f32_16x16x128_f8f6f4 v[54:57], v[26:33], v[212:219], v[54:57], v202, v202 op_sel_hi:[0,0,0]
	v_mfma_scale_f32_16x16x128_f8f6f4 v[50:53], v[18:25], v[220:227], v[50:53], v202, v202 op_sel_hi:[0,0,0]
	v_mfma_scale_f32_16x16x128_f8f6f4 v[46:49], v[26:33], v[220:227], v[46:49], v202, v202 op_sel_hi:[0,0,0]
	v_mfma_scale_f32_16x16x128_f8f6f4 v[42:45], v[18:25], v[228:235], v[42:45], v202, v202 op_sel_hi:[0,0,0]
	v_mfma_scale_f32_16x16x128_f8f6f4 v[38:41], v[26:33], v[228:235], v[38:41], v202, v202 op_sel_hi:[0,0,0]
	s_setprio 0
	s_barrier
; #define PG8_STAGE(bufoff, gbase, voff) do { _Pragma("unroll") for (int _i = 0; _i < 2; ++_i) \
;         __builtin_amdgcn_global_load_lds((const unsigned*)((const char*)(gbase) + (voff)[_i]), (PG8_LAS unsigned*)(lds + (bufoff) + ldsw + _i * 8192), 16, 0, 0); } while (0)
; #define PG8_LDA(dst, b, h) do { _Pragma("unroll") for (int m = 0; m < 4; ++m) _Pragma("unroll") for (int k = 0; k < 2; ++k) dst[m][k] = *(const PG8_LAS bf16x8*)(lds + PG8_SA(b, h) + aoff + m * 2048 + k * 1024); } while (0)
; #define PG8_LDB(dst, b, h) do { _Pragma("unroll") for (int n = 0; n < 2; ++n) _Pragma("unroll") for (int k = 0; k < 2; ++k) dst[n][k] = *(const PG8_LAS bf16x8*)(lds + PG8_SB(b, h) + boff + n * 2048 + k * 1024); } while (0)
; #define PG8_WAIT_V(n) asm volatile("s_waitcnt vmcnt(" #n ")" ::: "memory")
; #define PG8_WAIT_L(n) asm volatile("s_waitcnt lgkmcnt(" #n ")" ::: "memory")
; #define PG8_BAR __builtin_amdgcn_s_barrier()
; #define PG8_SCHED __builtin_amdgcn_sched_barrier(0)
;     ...
;         for (int t = 0; t < nt; t += 2) {
;     ...
;             PG8_LDB(B0, 1, 0); PG8_LDB(B1, 1, 1); PG8_SCHED; PG8_LDA(At, 1, 0); PG8_STAGE(PG8_SA(0, 1), a2 + hstepA, voffA);
;             PG8_WAIT_V(8); PG8_WAIT_L(0); PG8_BAR; PG8_MMA(0, 0, At, B0); PG8_MMA(0, 1, At, B1); PG8_BAR; PG8_SCHED;
;             PG8_LDA(At, 1, 1); PG8_STAGE(PG8_SB(1, 0), b3, voffB); PG8_STAGE(PG8_SB(1, 1), b3 + hstepB, voffB); PG8_STAGE(PG8_SA(1, 0), a3, voffA);
;             PG8_WAIT_V(8); PG8_WAIT_L(0); PG8_BAR; PG8_MMA(1, 0, At, B0); PG8_MMA(1, 1, At, B1); PG8_BAR; PG8_SCHED;
	s_add_i32 s71, 0, 0x18000
	s_add_i32 s76, 0, 0x1c000
	v_add_u32_e32 v2, s71, v198
	v_add_u32_e32 v6, s76, v198
	ds_read_b128 v[26:29], v2
	ds_read_b128 v[30:33], v2 offset:1024
	ds_read_b128 v[18:21], v2 offset:2048
	ds_read_b128 v[22:25], v2 offset:3072
	ds_read_b128 v[10:13], v6
	ds_read_b128 v[14:17], v6 offset:1024
	ds_read_b128 v[2:5], v6 offset:2048
	ds_read_b128 v[6:9], v6 offset:3072
	s_add_u32 s0, s30, 0x50000
	s_addc_u32 s1, s31, 0
	s_mov_b32 m0, s37
	v_lshl_add_u64 v[236:237], s[0:1], 0, v[166:167]
	ds_read_b128 v[204:207], v201 offset:32768
	ds_read_b128 v[208:211], v201 offset:33792
	ds_read_b128 v[212:215], v201 offset:34816
	ds_read_b128 v[216:219], v201 offset:35840
	ds_read_b128 v[220:223], v201 offset:36864
	ds_read_b128 v[224:227], v201 offset:37888
	ds_read_b128 v[228:231], v201 offset:38912
	ds_read_b128 v[232:235], v201 offset:39936
	global_load_lds_dwordx4 v[236:237], off
	v_lshl_add_u64 v[236:237], s[0:1], 0, v[170:171]
	s_mov_b32 m0, s38
	s_nop 0
	global_load_lds_dwordx4 v[236:237], off
	s_waitcnt vmcnt(8)
	s_waitcnt lgkmcnt(0)
	s_barrier
	s_setprio 1
	s_waitcnt lgkmcnt(0)
	v_mfma_scale_f32_16x16x128_f8f6f4 v[162:165], v[26:33], v[204:211], v[162:165], v202, v202 op_sel_hi:[0,0,0]
	v_mfma_scale_f32_16x16x128_f8f6f4 v[158:161], v[18:25], v[204:211], v[158:161], v202, v202 op_sel_hi:[0,0,0]
	v_mfma_scale_f32_16x16x128_f8f6f4 v[154:157], v[26:33], v[212:219], v[154:157], v202, v202 op_sel_hi:[0,0,0]
	v_mfma_scale_f32_16x16x128_f8f6f4 v[150:153], v[18:25], v[212:219], v[150:153], v202, v202 op_sel_hi:[0,0,0]
	v_mfma_scale_f32_16x16x128_f8f6f4 v[146:149], v[26:33], v[220:227], v[146:149], v202, v202 op_sel_hi:[0,0,0]
	v_mfma_scale_f32_16x16x128_f8f6f4 v[142:145], v[18:25], v[220:227], v[142:145], v202, v202 op_sel_hi:[0,0,0]
	v_mfma_scale_f32_16x16x128_f8f6f4 v[138:141], v[26:33], v[228:235], v[138:141], v202, v202 op_sel_hi:[0,0,0]
	v_mfma_scale_f32_16x16x128_f8f6f4 v[134:137], v[18:25], v[228:235], v[134:137], v202, v202 op_sel_hi:[0,0,0]
	s_setprio 0
	s_setprio 1
	v_mfma_scale_f32_16x16x128_f8f6f4 v[98:101], v[10:17], v[204:211], v[98:101], v202, v202 op_sel_hi:[0,0,0]
	v_mfma_scale_f32_16x16x128_f8f6f4 v[94:97], v[2:9], v[204:211], v[94:97], v202, v202 op_sel_hi:[0,0,0]
	v_mfma_scale_f32_16x16x128_f8f6f4 v[90:93], v[10:17], v[212:219], v[90:93], v202, v202 op_sel_hi:[0,0,0]
	v_mfma_scale_f32_16x16x128_f8f6f4 v[86:89], v[2:9], v[212:219], v[86:89], v202, v202 op_sel_hi:[0,0,0]
	v_mfma_scale_f32_16x16x128_f8f6f4 v[82:85], v[10:17], v[220:227], v[82:85], v202, v202 op_sel_hi:[0,0,0]
	v_mfma_scale_f32_16x16x128_f8f6f4 v[78:81], v[2:9], v[220:227], v[78:81], v202, v202 op_sel_hi:[0,0,0]
	v_mfma_scale_f32_16x16x128_f8f6f4 v[74:77], v[10:17], v[228:235], v[74:77], v202, v202 op_sel_hi:[0,0,0]
	v_mfma_scale_f32_16x16x128_f8f6f4 v[70:73], v[2:9], v[228:235], v[70:73], v202, v202 op_sel_hi:[0,0,0]
	s_setprio 0
	s_barrier
	s_add_i32 s0, s71, s10
	v_lshl_add_u64 v[36:37], v[36:37], 0, s[14:15]
	s_mov_b32 m0, s0
	ds_read_b128 v[204:207], v201 offset:49152
	ds_read_b128 v[208:211], v201 offset:50176
	ds_read_b128 v[212:215], v201 offset:51200
	ds_read_b128 v[216:219], v201 offset:52224
	ds_read_b128 v[220:223], v201 offset:53248
	ds_read_b128 v[224:227], v201 offset:54272
	ds_read_b128 v[228:231], v201 offset:55296
	ds_read_b128 v[232:235], v201 offset:56320
	global_load_lds_dwordx4 v[36:37], off
	s_add_i32 m0, s0, 0x2000
	s_add_u32 s0, s28, 0x50080
	v_lshl_add_u64 v[36:37], v[190:191], 0, s[14:15]
	s_addc_u32 s1, s29, 0
	s_add_i32 s28, s76, s10
	global_load_lds_dwordx4 v[36:37], off
	v_lshl_add_u64 v[36:37], s[0:1], 0, v[168:169]
	s_mov_b32 m0, s28
	s_nop 0
	global_load_lds_dwordx4 v[36:37], off
	v_lshl_add_u64 v[36:37], s[0:1], 0, v[172:173]
	s_add_i32 m0, s28, 0x2000
	s_nop 0
	global_load_lds_dwordx4 v[36:37], off
	v_lshl_add_u64 v[36:37], v[192:193], 0, s[14:15]
	s_mov_b32 m0, s43
	s_nop 0
	global_load_lds_dwordx4 v[36:37], off
	v_lshl_add_u64 v[36:37], v[194:195], 0, s[14:15]
	s_mov_b32 m0, s44
	s_nop 0
	global_load_lds_dwordx4 v[36:37], off
	s_waitcnt vmcnt(8)
	s_waitcnt lgkmcnt(0)
	s_barrier
	s_setprio 1
	s_waitcnt lgkmcnt(0)
	v_mfma_scale_f32_16x16x128_f8f6f4 v[130:133], v[26:33], v[204:211], v[130:133], v202, v202 op_sel_hi:[0,0,0]
	v_mfma_scale_f32_16x16x128_f8f6f4 v[126:129], v[18:25], v[204:211], v[126:129], v202, v202 op_sel_hi:[0,0,0]
	v_mfma_scale_f32_16x16x128_f8f6f4 v[122:125], v[26:33], v[212:219], v[122:125], v202, v202 op_sel_hi:[0,0,0]
	v_mfma_scale_f32_16x16x128_f8f6f4 v[118:121], v[18:25], v[212:219], v[118:121], v202, v202 op_sel_hi:[0,0,0]
	v_mfma_scale_f32_16x16x128_f8f6f4 v[114:117], v[26:33], v[220:227], v[114:117], v202, v202 op_sel_hi:[0,0,0]
	v_mfma_scale_f32_16x16x128_f8f6f4 v[110:113], v[18:25], v[220:227], v[110:113], v202, v202 op_sel_hi:[0,0,0]
	v_mfma_scale_f32_16x16x128_f8f6f4 v[106:109], v[26:33], v[228:235], v[106:109], v202, v202 op_sel_hi:[0,0,0]
	v_mfma_scale_f32_16x16x128_f8f6f4 v[102:105], v[18:25], v[228:235], v[102:105], v202, v202 op_sel_hi:[0,0,0]
	s_setprio 0
	s_setprio 1
	v_mfma_scale_f32_16x16x128_f8f6f4 v[66:69], v[10:17], v[204:211], v[66:69], v202, v202 op_sel_hi:[0,0,0]
	v_mfma_scale_f32_16x16x128_f8f6f4 v[62:65], v[2:9], v[204:211], v[62:65], v202, v202 op_sel_hi:[0,0,0]
	v_mfma_scale_f32_16x16x128_f8f6f4 v[58:61], v[10:17], v[212:219], v[58:61], v202, v202 op_sel_hi:[0,0,0]
	v_mfma_scale_f32_16x16x128_f8f6f4 v[54:57], v[2:9], v[212:219], v[54:57], v202, v202 op_sel_hi:[0,0,0]
	v_mfma_scale_f32_16x16x128_f8f6f4 v[50:53], v[10:17], v[220:227], v[50:53], v202, v202 op_sel_hi:[0,0,0]
	v_mfma_scale_f32_16x16x128_f8f6f4 v[46:49], v[2:9], v[220:227], v[46:49], v202, v202 op_sel_hi:[0,0,0]
	v_mfma_scale_f32_16x16x128_f8f6f4 v[42:45], v[10:17], v[228:235], v[42:45], v202, v202 op_sel_hi:[0,0,0]
	v_mfma_scale_f32_16x16x128_f8f6f4 v[38:41], v[2:9], v[228:235], v[38:41], v202, v202 op_sel_hi:[0,0,0]
	s_setprio 0
	s_add_i32 s70, s70, 2
	s_add_u32 s26, s26, 0x100
	s_addc_u32 s27, s27, 0
	s_cmp_gt_u32 s70, 17
	s_barrier
	s_cbranch_scc1 .LBB0_626

; #define PG8_STAGE(bufoff, gbase, voff) do { _Pragma("unroll") for (int _i = 0; _i < 2; ++_i) \
;         __builtin_amdgcn_global_load_lds((const unsigned*)((const char*)(gbase) + (voff)[_i]), (PG8_LAS unsigned*)(lds + (bufoff) + ldsw + _i * 8192), 16, 0, 0); } while (0)
; #define PG8_LDA(dst, b, h) do { _Pragma("unroll") for (int m = 0; m < 4; ++m) _Pragma("unroll") for (int k = 0; k < 2; ++k) dst[m][k] = *(const PG8_LAS bf16x8*)(lds + PG8_SA(b, h) + aoff + m * 2048 + k * 1024); } while (0)
; #define PG8_LDB(dst, b, h) do { _Pragma("unroll") for (int n = 0; n < 2; ++n) _Pragma("unroll") for (int k = 0; k < 2; ++k) dst[n][k] = *(const PG8_LAS bf16x8*)(lds + PG8_SB(b, h) + boff + n * 2048 + k * 1024); } while (0)
; #define PG8_WAIT_V(n) asm volatile("s_waitcnt vmcnt(" #n ")" ::: "memory")
; #define PG8_WAIT_L(n) asm volatile("s_waitcnt lgkmcnt(" #n ")" ::: "memory")
; #define PG8_BAR __builtin_amdgcn_s_barrier()
; #define PG8_SCHED __builtin_amdgcn_sched_barrier(0)
;     ...
;             const bool last = (t == nt - 2);
;             const char* a1 = cA + (size_t)(t + 1) * kstep;
;             const char* a2 = last ? nA : cA + (size_t)(t + 2) * kstep; const char* b2 = last ? nB : cB + (size_t)(t + 2) * kstep;
;             const char* a3 = a2 + kstep; const char* b3 = b2 + kstep;
;             if (last && has_next) S.a_ready(nxt);
;             if constexpr (Epi::MIDK > 0) { if (t == Epi::MIDK) {
;                 if constexpr (FP8) asm volatile("s_nop 15\n\ts_nop 15" ::: "memory");
;                 E.mid(acc, cur, wr, wc, fr, fq);
;                 if constexpr (FP8) asm volatile("s_nop 7" ::: "memory"); } }
;             if constexpr (SP2) {
;             PG8_LDB(B0, 0, 0); PG8_LDB(B1, 0, 1); PG8_SCHED; PG8_LDA(At, 0, 0); PG8_STAGE(PG8_SA(1, 1), a1 + hstepA, voffA);
;             PG8_WAIT_V(8); PG8_WAIT_L(0); PG8_BAR; PG8_MMA(0, 0, At, B0); PG8_MMA(0, 1, At, B1); PG8_BAR; PG8_SCHED;
;             PG8_LDA(At, 0, 1); PG8_STAGE(PG8_SB(0, 0), b2, voffB); PG8_STAGE(PG8_SB(0, 1), b2 + hstepB, voffB); PG8_STAGE(PG8_SA(0, 0), a2, voffA);
;             PG8_WAIT_V(8); PG8_WAIT_L(0); PG8_BAR; PG8_MMA(1, 0, At, B0); PG8_MMA(1, 1, At, B1); PG8_BAR; PG8_SCHED;
.LBB0_719:
	ds_read_b128 v[26:29], v189
	ds_read_b128 v[30:33], v189 offset:1024
	ds_read_b128 v[18:21], v189 offset:2048
	ds_read_b128 v[22:25], v189 offset:3072
	ds_read_b128 v[10:13], v190
	ds_read_b128 v[14:17], v190 offset:1024
	s_waitcnt lgkmcnt(0)
	ds_read_b128 v[2:5], v190 offset:2048
	ds_read_b128 v[6:9], v190 offset:3072
	s_add_u32 s42, s40, 0xfff80080
	s_addc_u32 s43, s41, -1
	s_cmp_eq_u32 s39, 28
	s_cselect_b32 s49, s0, s43
	s_cselect_b32 s48, s1, s42
	s_cselect_b32 s43, s20, s29
	s_cselect_b32 s42, s21, s27
	v_lshl_add_u64 v[218:219], s[40:41], 0, v[170:171]
	s_add_i32 m0, s35, 0xc000
	ds_read_b128 v[178:181], v191
	ds_read_b128 v[182:185], v191 offset:1024
	ds_read_b128 v[194:197], v191 offset:2048
	ds_read_b128 v[198:201], v191 offset:3072
	ds_read_b128 v[202:205], v191 offset:4096
	ds_read_b128 v[206:209], v191 offset:5120
	ds_read_b128 v[210:213], v191 offset:6144
	ds_read_b128 v[214:217], v191 offset:7168
	global_load_lds_dwordx4 v[218:219], off
	v_lshl_add_u64 v[218:219], s[40:41], 0, v[172:173]
	s_add_i32 m0, s35, 0xe000
	s_nop 0
	global_load_lds_dwordx4 v[218:219], off
	s_waitcnt vmcnt(8)
	s_waitcnt lgkmcnt(0)
	s_barrier
	s_setprio 1
	s_waitcnt lgkmcnt(0)
	v_mfma_scale_f32_16x16x128_f8f6f4 v[158:161], v[26:33], v[178:185], v[158:161], v192, v192 op_sel_hi:[0,0,0]
	v_mfma_scale_f32_16x16x128_f8f6f4 v[154:157], v[18:25], v[178:185], v[154:157], v192, v192 op_sel_hi:[0,0,0]
	v_mfma_scale_f32_16x16x128_f8f6f4 v[142:145], v[26:33], v[194:201], v[142:145], v192, v192 op_sel_hi:[0,0,0]
	v_mfma_scale_f32_16x16x128_f8f6f4 v[138:141], v[18:25], v[194:201], v[138:141], v192, v192 op_sel_hi:[0,0,0]
	v_mfma_scale_f32_16x16x128_f8f6f4 v[126:129], v[26:33], v[202:209], v[126:129], v192, v192 op_sel_hi:[0,0,0]
	v_mfma_scale_f32_16x16x128_f8f6f4 v[122:125], v[18:25], v[202:209], v[122:125], v192, v192 op_sel_hi:[0,0,0]
	v_mfma_scale_f32_16x16x128_f8f6f4 v[110:113], v[26:33], v[210:217], v[110:113], v192, v192 op_sel_hi:[0,0,0]
	v_mfma_scale_f32_16x16x128_f8f6f4 v[106:109], v[18:25], v[210:217], v[106:109], v192, v192 op_sel_hi:[0,0,0]
	s_setprio 0
	s_setprio 1
	v_mfma_scale_f32_16x16x128_f8f6f4 v[150:153], v[10:17], v[178:185], v[150:153], v192, v192 op_sel_hi:[0,0,0]
	v_mfma_scale_f32_16x16x128_f8f6f4 v[146:149], v[2:9], v[178:185], v[146:149], v192, v192 op_sel_hi:[0,0,0]
	v_mfma_scale_f32_16x16x128_f8f6f4 v[134:137], v[10:17], v[194:201], v[134:137], v192, v192 op_sel_hi:[0,0,0]
	v_mfma_scale_f32_16x16x128_f8f6f4 v[130:133], v[2:9], v[194:201], v[130:133], v192, v192 op_sel_hi:[0,0,0]
	v_mfma_scale_f32_16x16x128_f8f6f4 v[118:121], v[10:17], v[202:209], v[118:121], v192, v192 op_sel_hi:[0,0,0]
	v_mfma_scale_f32_16x16x128_f8f6f4 v[114:117], v[2:9], v[202:209], v[114:117], v192, v192 op_sel_hi:[0,0,0]
	v_mfma_scale_f32_16x16x128_f8f6f4 v[102:105], v[10:17], v[210:217], v[102:105], v192, v192 op_sel_hi:[0,0,0]
	v_mfma_scale_f32_16x16x128_f8f6f4 v[98:101], v[2:9], v[210:217], v[98:101], v192, v192 op_sel_hi:[0,0,0]
	s_setprio 0
	s_barrier
	s_add_i32 s72, s69, s11
	v_lshl_add_u64 v[178:179], s[42:43], 0, v[164:165]
	s_mov_b32 m0, s72
	ds_read_b128 v[194:197], v191 offset:16384
	ds_read_b128 v[198:201], v191 offset:17408
	ds_read_b128 v[202:205], v191 offset:18432
	ds_read_b128 v[206:209], v191 offset:19456
	ds_read_b128 v[210:213], v191 offset:20480
	ds_read_b128 v[214:217], v191 offset:21504
	ds_read_b128 v[218:221], v191 offset:22528
	ds_read_b128 v[222:225], v191 offset:23552
	global_load_lds_dwordx4 v[178:179], off
	s_add_i32 m0, s72, 0x2000
	s_add_u32 s72, s42, 0x80000
	v_lshl_add_u64 v[180:181], s[42:43], 0, v[168:169]
	s_addc_u32 s73, s43, 0
	s_add_i32 s74, s70, s11
	global_load_lds_dwordx4 v[180:181], off
	v_lshl_add_u64 v[182:183], s[72:73], 0, v[164:165]
	s_mov_b32 m0, s74
	v_lshl_add_u64 v[184:185], s[48:49], 0, v[166:167]
	global_load_lds_dwordx4 v[182:183], off
	v_lshl_add_u64 v[182:183], s[72:73], 0, v[168:169]
	s_add_i32 m0, s74, 0x2000
	s_nop 0
	global_load_lds_dwordx4 v[182:183], off
	v_lshl_add_u64 v[182:183], s[48:49], 0, v[162:163]
	s_mov_b32 m0, s35
	s_nop 0
	global_load_lds_dwordx4 v[182:183], off
	s_mov_b32 m0, s46
	s_nop 0
	global_load_lds_dwordx4 v[184:185], off
	s_waitcnt vmcnt(8)
	s_waitcnt lgkmcnt(0)
	s_barrier
	s_setprio 1
	s_waitcnt lgkmcnt(0)
	v_mfma_scale_f32_16x16x128_f8f6f4 v[94:97], v[26:33], v[194:201], v[94:97], v192, v192 op_sel_hi:[0,0,0]
	v_mfma_scale_f32_16x16x128_f8f6f4 v[90:93], v[18:25], v[194:201], v[90:93], v192, v192 op_sel_hi:[0,0,0]
	v_mfma_scale_f32_16x16x128_f8f6f4 v[78:81], v[26:33], v[202:209], v[78:81], v192, v192 op_sel_hi:[0,0,0]
	v_mfma_scale_f32_16x16x128_f8f6f4 v[74:77], v[18:25], v[202:209], v[74:77], v192, v192 op_sel_hi:[0,0,0]
	v_mfma_scale_f32_16x16x128_f8f6f4 v[62:65], v[26:33], v[210:217], v[62:65], v192, v192 op_sel_hi:[0,0,0]
	v_mfma_scale_f32_16x16x128_f8f6f4 v[58:61], v[18:25], v[210:217], v[58:61], v192, v192 op_sel_hi:[0,0,0]
	v_mfma_scale_f32_16x16x128_f8f6f4 v[46:49], v[26:33], v[218:225], v[46:49], v192, v192 op_sel_hi:[0,0,0]
	v_mfma_scale_f32_16x16x128_f8f6f4 v[42:45], v[18:25], v[218:225], v[42:45], v192, v192 op_sel_hi:[0,0,0]
	s_setprio 0
	s_setprio 1
	v_mfma_scale_f32_16x16x128_f8f6f4 v[86:89], v[10:17], v[194:201], v[86:89], v192, v192 op_sel_hi:[0,0,0]
	v_mfma_scale_f32_16x16x128_f8f6f4 v[82:85], v[2:9], v[194:201], v[82:85], v192, v192 op_sel_hi:[0,0,0]
	v_mfma_scale_f32_16x16x128_f8f6f4 v[70:73], v[10:17], v[202:209], v[70:73], v192, v192 op_sel_hi:[0,0,0]
	v_mfma_scale_f32_16x16x128_f8f6f4 v[66:69], v[2:9], v[202:209], v[66:69], v192, v192 op_sel_hi:[0,0,0]
	v_mfma_scale_f32_16x16x128_f8f6f4 v[54:57], v[10:17], v[210:217], v[54:57], v192, v192 op_sel_hi:[0,0,0]
	v_mfma_scale_f32_16x16x128_f8f6f4 v[50:53], v[2:9], v[210:217], v[50:53], v192, v192 op_sel_hi:[0,0,0]
	v_mfma_scale_f32_16x16x128_f8f6f4 v[38:41], v[10:17], v[218:225], v[38:41], v192, v192 op_sel_hi:[0,0,0]
	v_mfma_scale_f32_16x16x128_f8f6f4 v[34:37], v[2:9], v[218:225], v[34:37], v192, v192 op_sel_hi:[0,0,0]
	s_setprio 0
	s_barrier
; #define PG8_STAGE(bufoff, gbase, voff) do { _Pragma("unroll") for (int _i = 0; _i < 2; ++_i) \
;         __builtin_amdgcn_global_load_lds((const unsigned*)((const char*)(gbase) + (voff)[_i]), (PG8_LAS unsigned*)(lds + (bufoff) + ldsw + _i * 8192), 16, 0, 0); } while (0)
; #define PG8_LDA(dst, b, h) do { _Pragma("unroll") for (int m = 0; m < 4; ++m) _Pragma("unroll") for (int k = 0; k < 2; ++k) dst[m][k] = *(const PG8_LAS bf16x8*)(lds + PG8_SA(b, h) + aoff + m * 2048 + k * 1024); } while (0)
; #define PG8_LDB(dst, b, h) do { _Pragma("unroll") for (int n = 0; n < 2; ++n) _Pragma("unroll") for (int k = 0; k < 2; ++k) dst[n][k] = *(const PG8_LAS bf16x8*)(lds + PG8_SB(b, h) + boff + n * 2048 + k * 1024); } while (0)
; #define PG8_WAIT_V(n) asm volatile("s_waitcnt vmcnt(" #n ")" ::: "memory")
; #define PG8_WAIT_L(n) asm volatile("s_waitcnt lgkmcnt(" #n ")" ::: "memory")
; #define PG8_BAR __builtin_amdgcn_s_barrier()
; #define PG8_SCHED __builtin_amdgcn_sched_barrier(0)
;     ...
;             PG8_LDB(B0, 1, 0); PG8_LDB(B1, 1, 1); PG8_SCHED; PG8_LDA(At, 1, 0); PG8_STAGE(PG8_SA(0, 1), a2 + hstepA, voffA);
;             PG8_WAIT_V(8); PG8_WAIT_L(0); PG8_BAR; PG8_MMA(0, 0, At, B0); PG8_MMA(0, 1, At, B1); PG8_BAR; PG8_SCHED;
;             PG8_LDA(At, 1, 1); PG8_STAGE(PG8_SB(1, 0), b3, voffB); PG8_STAGE(PG8_SB(1, 1), b3 + hstepB, voffB); PG8_STAGE(PG8_SA(1, 0), a3, voffA);
;             PG8_WAIT_V(8); PG8_WAIT_L(0); PG8_BAR; PG8_MMA(1, 0, At, B0); PG8_MMA(1, 1, At, B1); PG8_BAR; PG8_SCHED;
;     ...
;         if constexpr (ALIGN_EPI) { if (wr == 0) PG8_BAR; }
	s_add_i32 s72, 0, 0x18000
	s_add_i32 s73, 0, 0x1c000
	v_add_u32_e32 v14, s72, v187
	v_add_u32_e32 v30, s73, v187
	ds_read_b128 v[2:5], v14
	ds_read_b128 v[6:9], v14 offset:1024
	ds_read_b128 v[10:13], v14 offset:2048
	ds_read_b128 v[14:17], v14 offset:3072
	ds_read_b128 v[18:21], v30
	ds_read_b128 v[22:25], v30 offset:1024
	ds_read_b128 v[26:29], v30 offset:2048
	ds_read_b128 v[30:33], v30 offset:3072
	s_add_u32 s48, s48, 0x80000
	s_addc_u32 s49, s49, 0
	s_mov_b32 m0, s47
	v_lshl_add_u64 v[226:227], s[48:49], 0, v[162:163]
	ds_read_b128 v[194:197], v191 offset:32768
	ds_read_b128 v[198:201], v191 offset:33792
	ds_read_b128 v[202:205], v191 offset:34816
	ds_read_b128 v[206:209], v191 offset:35840
	ds_read_b128 v[210:213], v191 offset:36864
	ds_read_b128 v[214:217], v191 offset:37888
	ds_read_b128 v[218:221], v191 offset:38912
	ds_read_b128 v[222:225], v191 offset:39936
	global_load_lds_dwordx4 v[226:227], off
	v_lshl_add_u64 v[226:227], s[48:49], 0, v[166:167]
	s_mov_b32 m0, s62
	s_nop 0
	global_load_lds_dwordx4 v[226:227], off
	s_waitcnt vmcnt(8)
	s_waitcnt lgkmcnt(0)
	s_barrier
	s_setprio 1
	s_waitcnt lgkmcnt(0)
	v_mfma_scale_f32_16x16x128_f8f6f4 v[158:161], v[2:9], v[194:201], v[158:161], v192, v192 op_sel_hi:[0,0,0]
	v_mfma_scale_f32_16x16x128_f8f6f4 v[154:157], v[10:17], v[194:201], v[154:157], v192, v192 op_sel_hi:[0,0,0]
	v_mfma_scale_f32_16x16x128_f8f6f4 v[142:145], v[2:9], v[202:209], v[142:145], v192, v192 op_sel_hi:[0,0,0]
	v_mfma_scale_f32_16x16x128_f8f6f4 v[138:141], v[10:17], v[202:209], v[138:141], v192, v192 op_sel_hi:[0,0,0]
	v_mfma_scale_f32_16x16x128_f8f6f4 v[126:129], v[2:9], v[210:217], v[126:129], v192, v192 op_sel_hi:[0,0,0]
	v_mfma_scale_f32_16x16x128_f8f6f4 v[122:125], v[10:17], v[210:217], v[122:125], v192, v192 op_sel_hi:[0,0,0]
	v_mfma_scale_f32_16x16x128_f8f6f4 v[110:113], v[2:9], v[218:225], v[110:113], v192, v192 op_sel_hi:[0,0,0]
	v_mfma_scale_f32_16x16x128_f8f6f4 v[106:109], v[10:17], v[218:225], v[106:109], v192, v192 op_sel_hi:[0,0,0]
	s_setprio 0
	s_setprio 1
	v_mfma_scale_f32_16x16x128_f8f6f4 v[150:153], v[18:25], v[194:201], v[150:153], v192, v192 op_sel_hi:[0,0,0]
	v_mfma_scale_f32_16x16x128_f8f6f4 v[146:149], v[26:33], v[194:201], v[146:149], v192, v192 op_sel_hi:[0,0,0]
	v_mfma_scale_f32_16x16x128_f8f6f4 v[134:137], v[18:25], v[202:209], v[134:137], v192, v192 op_sel_hi:[0,0,0]
	v_mfma_scale_f32_16x16x128_f8f6f4 v[130:133], v[26:33], v[202:209], v[130:133], v192, v192 op_sel_hi:[0,0,0]
	v_mfma_scale_f32_16x16x128_f8f6f4 v[118:121], v[18:25], v[210:217], v[118:121], v192, v192 op_sel_hi:[0,0,0]
	v_mfma_scale_f32_16x16x128_f8f6f4 v[114:117], v[26:33], v[210:217], v[114:117], v192, v192 op_sel_hi:[0,0,0]
	v_mfma_scale_f32_16x16x128_f8f6f4 v[102:105], v[18:25], v[218:225], v[102:105], v192, v192 op_sel_hi:[0,0,0]
	v_mfma_scale_f32_16x16x128_f8f6f4 v[98:101], v[26:33], v[218:225], v[98:101], v192, v192 op_sel_hi:[0,0,0]
	s_setprio 0
	s_barrier
	s_add_i32 s48, s72, s11
	v_lshl_add_u64 v[178:179], v[178:179], 0, s[22:23]
	s_mov_b32 m0, s48
	ds_read_b128 v[194:197], v191 offset:49152
	ds_read_b128 v[198:201], v191 offset:50176
	ds_read_b128 v[202:205], v191 offset:51200
	ds_read_b128 v[206:209], v191 offset:52224
	ds_read_b128 v[210:213], v191 offset:53248
	ds_read_b128 v[214:217], v191 offset:54272
	ds_read_b128 v[218:221], v191 offset:55296
	ds_read_b128 v[222:225], v191 offset:56320
	global_load_lds_dwordx4 v[178:179], off
	s_add_i32 m0, s48, 0x2000
	s_add_u32 s42, s42, 0x80080
	v_lshl_add_u64 v[178:179], v[180:181], 0, s[22:23]
	s_addc_u32 s43, s43, 0
	s_add_i32 s48, s73, s11
	global_load_lds_dwordx4 v[178:179], off
	v_lshl_add_u64 v[178:179], s[42:43], 0, v[164:165]
	s_mov_b32 m0, s48
	s_nop 0
	global_load_lds_dwordx4 v[178:179], off
	v_lshl_add_u64 v[178:179], s[42:43], 0, v[168:169]
	s_add_i32 m0, s48, 0x2000
	s_nop 0
	global_load_lds_dwordx4 v[178:179], off
	v_lshl_add_u64 v[178:179], v[182:183], 0, s[22:23]
	s_mov_b32 m0, s67
	s_nop 0
	global_load_lds_dwordx4 v[178:179], off
	v_lshl_add_u64 v[178:179], v[184:185], 0, s[22:23]
	s_mov_b32 m0, s68
	s_nop 0
	global_load_lds_dwordx4 v[178:179], off
	s_waitcnt vmcnt(8)
	s_waitcnt lgkmcnt(0)
	s_barrier
	s_setprio 1
	s_waitcnt lgkmcnt(0)
	v_mfma_scale_f32_16x16x128_f8f6f4 v[94:97], v[2:9], v[194:201], v[94:97], v192, v192 op_sel_hi:[0,0,0]
	v_mfma_scale_f32_16x16x128_f8f6f4 v[90:93], v[10:17], v[194:201], v[90:93], v192, v192 op_sel_hi:[0,0,0]
	v_mfma_scale_f32_16x16x128_f8f6f4 v[78:81], v[2:9], v[202:209], v[78:81], v192, v192 op_sel_hi:[0,0,0]
	v_mfma_scale_f32_16x16x128_f8f6f4 v[74:77], v[10:17], v[202:209], v[74:77], v192, v192 op_sel_hi:[0,0,0]
	v_mfma_scale_f32_16x16x128_f8f6f4 v[62:65], v[2:9], v[210:217], v[62:65], v192, v192 op_sel_hi:[0,0,0]
	v_mfma_scale_f32_16x16x128_f8f6f4 v[58:61], v[10:17], v[210:217], v[58:61], v192, v192 op_sel_hi:[0,0,0]
	v_mfma_scale_f32_16x16x128_f8f6f4 v[46:49], v[2:9], v[218:225], v[46:49], v192, v192 op_sel_hi:[0,0,0]
	v_mfma_scale_f32_16x16x128_f8f6f4 v[42:45], v[10:17], v[218:225], v[42:45], v192, v192 op_sel_hi:[0,0,0]
	s_setprio 0
	s_setprio 1
	v_mfma_scale_f32_16x16x128_f8f6f4 v[86:89], v[18:25], v[194:201], v[86:89], v192, v192 op_sel_hi:[0,0,0]
	v_mfma_scale_f32_16x16x128_f8f6f4 v[82:85], v[26:33], v[194:201], v[82:85], v192, v192 op_sel_hi:[0,0,0]
	v_mfma_scale_f32_16x16x128_f8f6f4 v[70:73], v[18:25], v[202:209], v[70:73], v192, v192 op_sel_hi:[0,0,0]
	v_mfma_scale_f32_16x16x128_f8f6f4 v[66:69], v[26:33], v[202:209], v[66:69], v192, v192 op_sel_hi:[0,0,0]
	v_mfma_scale_f32_16x16x128_f8f6f4 v[54:57], v[18:25], v[210:217], v[54:57], v192, v192 op_sel_hi:[0,0,0]
	v_mfma_scale_f32_16x16x128_f8f6f4 v[50:53], v[26:33], v[210:217], v[50:53], v192, v192 op_sel_hi:[0,0,0]
	v_mfma_scale_f32_16x16x128_f8f6f4 v[38:41], v[18:25], v[218:225], v[38:41], v192, v192 op_sel_hi:[0,0,0]
	v_mfma_scale_f32_16x16x128_f8f6f4 v[34:37], v[26:33], v[218:225], v[34:37], v192, v192 op_sel_hi:[0,0,0]
	s_setprio 0
	s_add_i32 s39, s39, 2
	s_add_u32 s40, s40, 0x100
	s_addc_u32 s41, s41, 0
	s_add_u32 s27, s27, 0x100
	s_addc_u32 s29, s29, 0
	s_cmp_gt_u32 s39, 29
	s_barrier
	s_cbranch_scc0 .LBB0_719
	s_and_b64 vcc, exec, s[24:25]
	s_cbranch_vccz .LBB0_722
	s_barrier

; #define PG8_STAGE(bufoff, gbase, voff) do { _Pragma("unroll") for (int _i = 0; _i < 2; ++_i) \
;         __builtin_amdgcn_global_load_lds((const unsigned*)((const char*)(gbase) + (voff)[_i]), (PG8_LAS unsigned*)(lds + (bufoff) + ldsw + _i * 8192), 16, 0, 0); } while (0)
; #define PG8_LDA(dst, b, h) do { _Pragma("unroll") for (int m = 0; m < 4; ++m) _Pragma("unroll") for (int k = 0; k < 2; ++k) dst[m][k] = *(const PG8_LAS bf16x8*)(lds + PG8_SA(b, h) + aoff + m * 2048 + k * 1024); } while (0)
; #define PG8_LDB(dst, b, h) do { _Pragma("unroll") for (int n = 0; n < 2; ++n) _Pragma("unroll") for (int k = 0; k < 2; ++k) dst[n][k] = *(const PG8_LAS bf16x8*)(lds + PG8_SB(b, h) + boff + n * 2048 + k * 1024); } while (0)
; #define PG8_WAIT_V(n) asm volatile("s_waitcnt vmcnt(" #n ")" ::: "memory")
; #define PG8_WAIT_L(n) asm volatile("s_waitcnt lgkmcnt(" #n ")" ::: "memory")
; #define PG8_BAR __builtin_amdgcn_s_barrier()
; #define PG8_SCHED __builtin_amdgcn_sched_barrier(0)
;     ...
;             const bool last = (t == nt - 2);
;             const char* a1 = cA + (size_t)(t + 1) * kstep;
;             const char* a2 = last ? nA : cA + (size_t)(t + 2) * kstep; const char* b2 = last ? nB : cB + (size_t)(t + 2) * kstep;
;             const char* a3 = a2 + kstep; const char* b3 = b2 + kstep;
;             if (last && has_next) S.a_ready(nxt);
;             if constexpr (Epi::MIDK > 0) { if (t == Epi::MIDK) {
;                 if constexpr (FP8) asm volatile("s_nop 15\n\ts_nop 15" ::: "memory");
;                 E.mid(acc, cur, wr, wc, fr, fq);
;                 if constexpr (FP8) asm volatile("s_nop 7" ::: "memory"); } }
;             if constexpr (SP2) {
;             PG8_LDB(B0, 0, 0); PG8_LDB(B1, 0, 1); PG8_SCHED; PG8_LDA(At, 0, 0); PG8_STAGE(PG8_SA(1, 1), a1 + hstepA, voffA);
;             PG8_WAIT_V(8); PG8_WAIT_L(0); PG8_BAR; PG8_MMA(0, 0, At, B0); PG8_MMA(0, 1, At, B1); PG8_BAR; PG8_SCHED;
;             PG8_LDA(At, 0, 1); PG8_STAGE(PG8_SB(0, 0), b2, voffB); PG8_STAGE(PG8_SB(0, 1), b2 + hstepB, voffB); PG8_STAGE(PG8_SA(0, 0), a2, voffA);
;             PG8_WAIT_V(8); PG8_WAIT_L(0); PG8_BAR; PG8_MMA(1, 0, At, B0); PG8_MMA(1, 1, At, B1); PG8_BAR; PG8_SCHED;
.LBB0_828:
	ds_read_b128 v[176:179], v172
	ds_read_b128 v[180:183], v172 offset:1024
	ds_read_b128 v[184:187], v172 offset:2048
	ds_read_b128 v[188:191], v172 offset:3072
	ds_read_b128 v[192:195], v173
	ds_read_b128 v[196:199], v173 offset:1024
	ds_read_b128 v[200:203], v173 offset:2048
	ds_read_b128 v[204:207], v173 offset:3072
	s_add_u32 s24, s22, 0xfff00080
	s_addc_u32 s25, s23, -1
	s_cmp_eq_u32 s47, 60
	s_cselect_b32 s27, s15, s25
	s_cselect_b32 s26, s41, s24
	s_cselect_b32 s25, s13, s46
	s_cselect_b32 s24, s42, s43
	v_lshl_add_u64 v[146:147], s[22:23], 0, v[138:139]
	s_add_i32 m0, s21, 0xc000
	ds_read_b128 v[208:211], v174
	ds_read_b128 v[212:215], v174 offset:1024
	ds_read_b128 v[216:219], v174 offset:2048
	ds_read_b128 v[220:223], v174 offset:3072
	ds_read_b128 v[224:227], v174 offset:4096
	ds_read_b128 v[228:231], v174 offset:5120
	ds_read_b128 v[232:235], v174 offset:6144
	ds_read_b128 v[236:239], v174 offset:7168
	global_load_lds_dwordx4 v[146:147], off
	v_lshl_add_u64 v[146:147], s[22:23], 0, v[140:141]
	s_add_i32 m0, s21, 0xe000
	s_nop 0
	global_load_lds_dwordx4 v[146:147], off
	s_waitcnt vmcnt(8)
	s_waitcnt lgkmcnt(0)
	s_barrier
	s_setprio 1
	s_waitcnt lgkmcnt(0)
	v_mfma_f32_16x16x32_bf16 v[126:129], v[176:179], v[208:211], v[126:129]
	v_mfma_f32_16x16x32_bf16 v[122:125], v[184:187], v[208:211], v[122:125]
	v_mfma_f32_16x16x32_bf16 v[118:121], v[176:179], v[216:219], v[118:121]
	v_mfma_f32_16x16x32_bf16 v[114:117], v[184:187], v[216:219], v[114:117]
	v_mfma_f32_16x16x32_bf16 v[102:105], v[176:179], v[224:227], v[102:105]
	v_mfma_f32_16x16x32_bf16 v[98:101], v[184:187], v[224:227], v[98:101]
	v_mfma_f32_16x16x32_bf16 v[86:89], v[176:179], v[232:235], v[86:89]
	v_mfma_f32_16x16x32_bf16 v[82:85], v[184:187], v[232:235], v[82:85]
	v_mfma_f32_16x16x32_bf16 v[126:129], v[180:183], v[212:215], v[126:129]
	v_mfma_f32_16x16x32_bf16 v[122:125], v[188:191], v[212:215], v[122:125]
	v_mfma_f32_16x16x32_bf16 v[118:121], v[180:183], v[220:223], v[118:121]
	v_mfma_f32_16x16x32_bf16 v[114:117], v[188:191], v[220:223], v[114:117]
	v_mfma_f32_16x16x32_bf16 v[102:105], v[180:183], v[228:231], v[102:105]
	v_mfma_f32_16x16x32_bf16 v[98:101], v[188:191], v[228:231], v[98:101]
	v_mfma_f32_16x16x32_bf16 v[86:89], v[180:183], v[236:239], v[86:89]
	v_mfma_f32_16x16x32_bf16 v[82:85], v[188:191], v[236:239], v[82:85]
	s_setprio 0
	s_setprio 1
	v_mfma_f32_16x16x32_bf16 v[110:113], v[192:195], v[208:211], v[110:113]
	v_mfma_f32_16x16x32_bf16 v[106:109], v[200:203], v[208:211], v[106:109]
	v_mfma_f32_16x16x32_bf16 v[94:97], v[192:195], v[216:219], v[94:97]
	v_mfma_f32_16x16x32_bf16 v[90:93], v[200:203], v[216:219], v[90:93]
	v_mfma_f32_16x16x32_bf16 v[78:81], v[192:195], v[224:227], v[78:81]
	v_mfma_f32_16x16x32_bf16 v[74:77], v[200:203], v[224:227], v[74:77]
	v_mfma_f32_16x16x32_bf16 v[70:73], v[192:195], v[232:235], v[70:73]
	v_mfma_f32_16x16x32_bf16 v[66:69], v[200:203], v[232:235], v[66:69]
	v_mfma_f32_16x16x32_bf16 v[110:113], v[196:199], v[212:215], v[110:113]
	v_mfma_f32_16x16x32_bf16 v[106:109], v[204:207], v[212:215], v[106:109]
	v_mfma_f32_16x16x32_bf16 v[94:97], v[196:199], v[220:223], v[94:97]
	v_mfma_f32_16x16x32_bf16 v[90:93], v[204:207], v[220:223], v[90:93]
	v_mfma_f32_16x16x32_bf16 v[78:81], v[196:199], v[228:231], v[78:81]
	v_mfma_f32_16x16x32_bf16 v[74:77], v[204:207], v[228:231], v[74:77]
	v_mfma_f32_16x16x32_bf16 v[70:73], v[196:199], v[236:239], v[70:73]
	v_mfma_f32_16x16x32_bf16 v[66:69], v[204:207], v[236:239], v[66:69]
	s_setprio 0
	s_barrier
	s_add_i32 s48, s38, s11
	v_lshl_add_u64 v[146:147], s[24:25], 0, v[132:133]
	s_mov_b32 m0, s48
	ds_read_b128 v[208:211], v174 offset:16384
	ds_read_b128 v[212:215], v174 offset:17408
	ds_read_b128 v[216:219], v174 offset:18432
	ds_read_b128 v[220:223], v174 offset:19456
	ds_read_b128 v[224:227], v174 offset:20480
	ds_read_b128 v[228:231], v174 offset:21504
	ds_read_b128 v[232:235], v174 offset:22528
	ds_read_b128 v[236:239], v174 offset:23552
	global_load_lds_dwordx4 v[146:147], off
	s_add_i32 m0, s48, 0x2000
	s_add_u32 s48, s24, 0x100000
	v_lshl_add_u64 v[150:151], s[24:25], 0, v[136:137]
	s_addc_u32 s49, s25, 0
	s_add_i32 s62, s39, s11
	global_load_lds_dwordx4 v[150:151], off
	v_lshl_add_u64 v[240:241], s[48:49], 0, v[132:133]
	s_mov_b32 m0, s62
	v_lshl_add_u64 v[242:243], s[26:27], 0, v[134:135]
	global_load_lds_dwordx4 v[240:241], off
	v_lshl_add_u64 v[240:241], s[48:49], 0, v[136:137]
	s_add_i32 m0, s62, 0x2000
	s_nop 0
	global_load_lds_dwordx4 v[240:241], off
	v_lshl_add_u64 v[240:241], s[26:27], 0, v[130:131]
	s_mov_b32 m0, s21
	s_nop 0
	global_load_lds_dwordx4 v[240:241], off
	s_mov_b32 m0, s30
	s_nop 0
	global_load_lds_dwordx4 v[242:243], off
	s_waitcnt vmcnt(8)
	s_waitcnt lgkmcnt(0)
	s_barrier
; #define PG8_STAGE(bufoff, gbase, voff) do { _Pragma("unroll") for (int _i = 0; _i < 2; ++_i) \
;         __builtin_amdgcn_global_load_lds((const unsigned*)((const char*)(gbase) + (voff)[_i]), (PG8_LAS unsigned*)(lds + (bufoff) + ldsw + _i * 8192), 16, 0, 0); } while (0)
; #define PG8_LDA(dst, b, h) do { _Pragma("unroll") for (int m = 0; m < 4; ++m) _Pragma("unroll") for (int k = 0; k < 2; ++k) dst[m][k] = *(const PG8_LAS bf16x8*)(lds + PG8_SA(b, h) + aoff + m * 2048 + k * 1024); } while (0)
; #define PG8_LDB(dst, b, h) do { _Pragma("unroll") for (int n = 0; n < 2; ++n) _Pragma("unroll") for (int k = 0; k < 2; ++k) dst[n][k] = *(const PG8_LAS bf16x8*)(lds + PG8_SB(b, h) + boff + n * 2048 + k * 1024); } while (0)
; #define PG8_WAIT_V(n) asm volatile("s_waitcnt vmcnt(" #n ")" ::: "memory")
; #define PG8_WAIT_L(n) asm volatile("s_waitcnt lgkmcnt(" #n ")" ::: "memory")
; #define PG8_BAR __builtin_amdgcn_s_barrier()
; #define PG8_SCHED __builtin_amdgcn_sched_barrier(0)
;     ...
;             PG8_WAIT_V(8); PG8_WAIT_L(0); PG8_BAR; PG8_MMA(1, 0, At, B0); PG8_MMA(1, 1, At, B1); PG8_BAR; PG8_SCHED;
;             PG8_LDB(B0, 1, 0); PG8_LDB(B1, 1, 1); PG8_SCHED; PG8_LDA(At, 1, 0); PG8_STAGE(PG8_SA(0, 1), a2 + hstepA, voffA);
;             PG8_WAIT_V(8); PG8_WAIT_L(0); PG8_BAR; PG8_MMA(0, 0, At, B0); PG8_MMA(0, 1, At, B1); PG8_BAR; PG8_SCHED;
	s_setprio 1
	s_waitcnt lgkmcnt(0)
	v_mfma_f32_16x16x32_bf16 v[62:65], v[176:179], v[208:211], v[62:65]
	v_mfma_f32_16x16x32_bf16 v[58:61], v[184:187], v[208:211], v[58:61]
	v_mfma_f32_16x16x32_bf16 v[54:57], v[176:179], v[216:219], v[54:57]
	v_mfma_f32_16x16x32_bf16 v[50:53], v[184:187], v[216:219], v[50:53]
	v_mfma_f32_16x16x32_bf16 v[38:41], v[176:179], v[224:227], v[38:41]
	v_mfma_f32_16x16x32_bf16 v[34:37], v[184:187], v[224:227], v[34:37]
	v_mfma_f32_16x16x32_bf16 v[22:25], v[176:179], v[232:235], v[22:25]
	v_mfma_f32_16x16x32_bf16 v[14:17], v[184:187], v[232:235], v[14:17]
	v_mfma_f32_16x16x32_bf16 v[62:65], v[180:183], v[212:215], v[62:65]
	v_mfma_f32_16x16x32_bf16 v[58:61], v[188:191], v[212:215], v[58:61]
	v_mfma_f32_16x16x32_bf16 v[54:57], v[180:183], v[220:223], v[54:57]
	v_mfma_f32_16x16x32_bf16 v[50:53], v[188:191], v[220:223], v[50:53]
	v_mfma_f32_16x16x32_bf16 v[38:41], v[180:183], v[228:231], v[38:41]
	v_mfma_f32_16x16x32_bf16 v[34:37], v[188:191], v[228:231], v[34:37]
	v_mfma_f32_16x16x32_bf16 v[22:25], v[180:183], v[236:239], v[22:25]
	v_mfma_f32_16x16x32_bf16 v[14:17], v[188:191], v[236:239], v[14:17]
	s_setprio 0
	s_setprio 1
	v_mfma_f32_16x16x32_bf16 v[46:49], v[192:195], v[208:211], v[46:49]
	v_mfma_f32_16x16x32_bf16 v[42:45], v[200:203], v[208:211], v[42:45]
	v_mfma_f32_16x16x32_bf16 v[30:33], v[192:195], v[216:219], v[30:33]
	v_mfma_f32_16x16x32_bf16 v[26:29], v[200:203], v[216:219], v[26:29]
	v_mfma_f32_16x16x32_bf16 v[18:21], v[192:195], v[224:227], v[18:21]
	v_mfma_f32_16x16x32_bf16 v[10:13], v[200:203], v[224:227], v[10:13]
	v_mfma_f32_16x16x32_bf16 v[6:9], v[192:195], v[232:235], v[6:9]
	v_mfma_f32_16x16x32_bf16 v[2:5], v[200:203], v[232:235], v[2:5]
	v_mfma_f32_16x16x32_bf16 v[46:49], v[196:199], v[212:215], v[46:49]
	v_mfma_f32_16x16x32_bf16 v[42:45], v[204:207], v[212:215], v[42:45]
	v_mfma_f32_16x16x32_bf16 v[30:33], v[196:199], v[220:223], v[30:33]
	v_mfma_f32_16x16x32_bf16 v[26:29], v[204:207], v[220:223], v[26:29]
	v_mfma_f32_16x16x32_bf16 v[18:21], v[196:199], v[228:231], v[18:21]
	v_mfma_f32_16x16x32_bf16 v[10:13], v[204:207], v[228:231], v[10:13]
	v_mfma_f32_16x16x32_bf16 v[6:9], v[196:199], v[236:239], v[6:9]
	v_mfma_f32_16x16x32_bf16 v[2:5], v[204:207], v[236:239], v[2:5]
	s_setprio 0
	s_barrier
	s_add_i32 s48, 0, 0x18000
	v_add_u32_e32 v148, s48, v153
	s_add_i32 s49, 0, 0x1c000
	ds_read_b128 v[176:179], v148
	ds_read_b128 v[180:183], v148 offset:1024
	ds_read_b128 v[184:187], v148 offset:2048
	ds_read_b128 v[188:191], v148 offset:3072
	v_add_u32_e32 v148, s49, v153
	ds_read_b128 v[192:195], v148
	ds_read_b128 v[196:199], v148 offset:1024
	ds_read_b128 v[200:203], v148 offset:2048
	ds_read_b128 v[204:207], v148 offset:3072
	s_add_u32 s26, s26, 0x100000
	s_addc_u32 s27, s27, 0
	s_mov_b32 m0, s31
	v_lshl_add_u64 v[244:245], s[26:27], 0, v[130:131]
	ds_read_b128 v[208:211], v174 offset:32768
	ds_read_b128 v[212:215], v174 offset:33792
	ds_read_b128 v[216:219], v174 offset:34816
	ds_read_b128 v[220:223], v174 offset:35840
	ds_read_b128 v[224:227], v174 offset:36864
	ds_read_b128 v[228:231], v174 offset:37888
	ds_read_b128 v[232:235], v174 offset:38912
	ds_read_b128 v[236:239], v174 offset:39936
	global_load_lds_dwordx4 v[244:245], off
	v_lshl_add_u64 v[244:245], s[26:27], 0, v[134:135]
	s_mov_b32 m0, s33
	s_nop 0
	global_load_lds_dwordx4 v[244:245], off
	s_waitcnt vmcnt(8)
	s_waitcnt lgkmcnt(0)
	s_barrier
	s_setprio 1
	s_waitcnt lgkmcnt(0)
	v_mfma_f32_16x16x32_bf16 v[126:129], v[176:179], v[208:211], v[126:129]
	v_mfma_f32_16x16x32_bf16 v[122:125], v[184:187], v[208:211], v[122:125]
	v_mfma_f32_16x16x32_bf16 v[118:121], v[176:179], v[216:219], v[118:121]
	v_mfma_f32_16x16x32_bf16 v[114:117], v[184:187], v[216:219], v[114:117]
	v_mfma_f32_16x16x32_bf16 v[102:105], v[176:179], v[224:227], v[102:105]
	v_mfma_f32_16x16x32_bf16 v[98:101], v[184:187], v[224:227], v[98:101]
	v_mfma_f32_16x16x32_bf16 v[86:89], v[176:179], v[232:235], v[86:89]
	v_mfma_f32_16x16x32_bf16 v[82:85], v[184:187], v[232:235], v[82:85]
	v_mfma_f32_16x16x32_bf16 v[126:129], v[180:183], v[212:215], v[126:129]
	v_mfma_f32_16x16x32_bf16 v[122:125], v[188:191], v[212:215], v[122:125]
	v_mfma_f32_16x16x32_bf16 v[118:121], v[180:183], v[220:223], v[118:121]
	v_mfma_f32_16x16x32_bf16 v[114:117], v[188:191], v[220:223], v[114:117]
	v_mfma_f32_16x16x32_bf16 v[102:105], v[180:183], v[228:231], v[102:105]
	v_mfma_f32_16x16x32_bf16 v[98:101], v[188:191], v[228:231], v[98:101]
	v_mfma_f32_16x16x32_bf16 v[86:89], v[180:183], v[236:239], v[86:89]
	v_mfma_f32_16x16x32_bf16 v[82:85], v[188:191], v[236:239], v[82:85]
	s_setprio 0
	s_setprio 1
	v_mfma_f32_16x16x32_bf16 v[110:113], v[192:195], v[208:211], v[110:113]
	v_mfma_f32_16x16x32_bf16 v[106:109], v[200:203], v[208:211], v[106:109]
	v_mfma_f32_16x16x32_bf16 v[94:97], v[192:195], v[216:219], v[94:97]
	v_mfma_f32_16x16x32_bf16 v[90:93], v[200:203], v[216:219], v[90:93]
	v_mfma_f32_16x16x32_bf16 v[78:81], v[192:195], v[224:227], v[78:81]
	v_mfma_f32_16x16x32_bf16 v[74:77], v[200:203], v[224:227], v[74:77]
	v_mfma_f32_16x16x32_bf16 v[70:73], v[192:195], v[232:235], v[70:73]
	v_mfma_f32_16x16x32_bf16 v[66:69], v[200:203], v[232:235], v[66:69]
	v_mfma_f32_16x16x32_bf16 v[110:113], v[196:199], v[212:215], v[110:113]
	v_mfma_f32_16x16x32_bf16 v[106:109], v[204:207], v[212:215], v[106:109]
	v_mfma_f32_16x16x32_bf16 v[94:97], v[196:199], v[220:223], v[94:97]
	v_mfma_f32_16x16x32_bf16 v[90:93], v[204:207], v[220:223], v[90:93]
	v_mfma_f32_16x16x32_bf16 v[78:81], v[196:199], v[228:231], v[78:81]
	v_mfma_f32_16x16x32_bf16 v[74:77], v[204:207], v[228:231], v[74:77]
	v_mfma_f32_16x16x32_bf16 v[70:73], v[196:199], v[236:239], v[70:73]
	v_mfma_f32_16x16x32_bf16 v[66:69], v[204:207], v[236:239], v[66:69]
	s_setprio 0
	s_barrier
; #define PG8_STAGE(bufoff, gbase, voff) do { _Pragma("unroll") for (int _i = 0; _i < 2; ++_i) \
;         __builtin_amdgcn_global_load_lds((const unsigned*)((const char*)(gbase) + (voff)[_i]), (PG8_LAS unsigned*)(lds + (bufoff) + ldsw + _i * 8192), 16, 0, 0); } while (0)
; #define PG8_LDA(dst, b, h) do { _Pragma("unroll") for (int m = 0; m < 4; ++m) _Pragma("unroll") for (int k = 0; k < 2; ++k) dst[m][k] = *(const PG8_LAS bf16x8*)(lds + PG8_SA(b, h) + aoff + m * 2048 + k * 1024); } while (0)
; #define PG8_WAIT_V(n) asm volatile("s_waitcnt vmcnt(" #n ")" ::: "memory")
; #define PG8_WAIT_L(n) asm volatile("s_waitcnt lgkmcnt(" #n ")" ::: "memory")
; #define PG8_BAR __builtin_amdgcn_s_barrier()
; #define PG8_SCHED __builtin_amdgcn_sched_barrier(0)
;     ...
;             PG8_LDA(At, 1, 1); PG8_STAGE(PG8_SB(1, 0), b3, voffB); PG8_STAGE(PG8_SB(1, 1), b3 + hstepB, voffB); PG8_STAGE(PG8_SA(1, 0), a3, voffA);
;             PG8_WAIT_V(8); PG8_WAIT_L(0); PG8_BAR; PG8_MMA(1, 0, At, B0); PG8_MMA(1, 1, At, B1); PG8_BAR; PG8_SCHED;
;     ...
;         if constexpr (ALIGN_EPI) { if (wr == 0) PG8_BAR; }
	s_add_i32 s26, s48, s11
	v_lshl_add_u64 v[146:147], v[146:147], 0, s[6:7]
	s_mov_b32 m0, s26
	ds_read_b128 v[208:211], v174 offset:49152
	ds_read_b128 v[212:215], v174 offset:50176
	ds_read_b128 v[216:219], v174 offset:51200
	ds_read_b128 v[220:223], v174 offset:52224
	ds_read_b128 v[224:227], v174 offset:53248
	ds_read_b128 v[228:231], v174 offset:54272
	ds_read_b128 v[232:235], v174 offset:55296
	ds_read_b128 v[236:239], v174 offset:56320
	global_load_lds_dwordx4 v[146:147], off
	s_add_i32 m0, s26, 0x2000
	s_add_u32 s24, s24, 0x100080
	v_lshl_add_u64 v[146:147], v[150:151], 0, s[6:7]
	s_addc_u32 s25, s25, 0
	s_add_i32 s26, s49, s11
	global_load_lds_dwordx4 v[146:147], off
	v_lshl_add_u64 v[146:147], s[24:25], 0, v[132:133]
	s_mov_b32 m0, s26
	s_nop 0
	global_load_lds_dwordx4 v[146:147], off
	v_lshl_add_u64 v[146:147], s[24:25], 0, v[136:137]
	s_add_i32 m0, s26, 0x2000
	s_nop 0
	global_load_lds_dwordx4 v[146:147], off
	v_lshl_add_u64 v[146:147], v[240:241], 0, s[6:7]
	s_mov_b32 m0, s36
	s_nop 0
	global_load_lds_dwordx4 v[146:147], off
	v_lshl_add_u64 v[146:147], v[242:243], 0, s[6:7]
	s_mov_b32 m0, s37
	s_nop 0
	global_load_lds_dwordx4 v[146:147], off
	s_waitcnt vmcnt(8)
	s_waitcnt lgkmcnt(0)
	s_barrier
	s_setprio 1
	s_waitcnt lgkmcnt(0)
	v_mfma_f32_16x16x32_bf16 v[62:65], v[176:179], v[208:211], v[62:65]
	v_mfma_f32_16x16x32_bf16 v[58:61], v[184:187], v[208:211], v[58:61]
	v_mfma_f32_16x16x32_bf16 v[54:57], v[176:179], v[216:219], v[54:57]
	v_mfma_f32_16x16x32_bf16 v[50:53], v[184:187], v[216:219], v[50:53]
	v_mfma_f32_16x16x32_bf16 v[38:41], v[176:179], v[224:227], v[38:41]
	v_mfma_f32_16x16x32_bf16 v[34:37], v[184:187], v[224:227], v[34:37]
	v_mfma_f32_16x16x32_bf16 v[22:25], v[176:179], v[232:235], v[22:25]
	v_mfma_f32_16x16x32_bf16 v[14:17], v[184:187], v[232:235], v[14:17]
	v_mfma_f32_16x16x32_bf16 v[62:65], v[180:183], v[212:215], v[62:65]
	v_mfma_f32_16x16x32_bf16 v[58:61], v[188:191], v[212:215], v[58:61]
	v_mfma_f32_16x16x32_bf16 v[54:57], v[180:183], v[220:223], v[54:57]
	v_mfma_f32_16x16x32_bf16 v[50:53], v[188:191], v[220:223], v[50:53]
	v_mfma_f32_16x16x32_bf16 v[38:41], v[180:183], v[228:231], v[38:41]
	v_mfma_f32_16x16x32_bf16 v[34:37], v[188:191], v[228:231], v[34:37]
	v_mfma_f32_16x16x32_bf16 v[22:25], v[180:183], v[236:239], v[22:25]
	v_mfma_f32_16x16x32_bf16 v[14:17], v[188:191], v[236:239], v[14:17]
	s_setprio 0
	s_setprio 1
	v_mfma_f32_16x16x32_bf16 v[46:49], v[192:195], v[208:211], v[46:49]
	v_mfma_f32_16x16x32_bf16 v[42:45], v[200:203], v[208:211], v[42:45]
	v_mfma_f32_16x16x32_bf16 v[30:33], v[192:195], v[216:219], v[30:33]
	v_mfma_f32_16x16x32_bf16 v[26:29], v[200:203], v[216:219], v[26:29]
	v_mfma_f32_16x16x32_bf16 v[18:21], v[192:195], v[224:227], v[18:21]
	v_mfma_f32_16x16x32_bf16 v[10:13], v[200:203], v[224:227], v[10:13]
	v_mfma_f32_16x16x32_bf16 v[6:9], v[192:195], v[232:235], v[6:9]
	v_mfma_f32_16x16x32_bf16 v[2:5], v[200:203], v[232:235], v[2:5]
	v_mfma_f32_16x16x32_bf16 v[46:49], v[196:199], v[212:215], v[46:49]
	v_mfma_f32_16x16x32_bf16 v[42:45], v[204:207], v[212:215], v[42:45]
	v_mfma_f32_16x16x32_bf16 v[30:33], v[196:199], v[220:223], v[30:33]
	v_mfma_f32_16x16x32_bf16 v[26:29], v[204:207], v[220:223], v[26:29]
	v_mfma_f32_16x16x32_bf16 v[18:21], v[196:199], v[228:231], v[18:21]
	v_mfma_f32_16x16x32_bf16 v[10:13], v[204:207], v[228:231], v[10:13]
	v_mfma_f32_16x16x32_bf16 v[6:9], v[196:199], v[236:239], v[6:9]
	v_mfma_f32_16x16x32_bf16 v[2:5], v[204:207], v[236:239], v[2:5]
	s_setprio 0
	s_add_i32 s47, s47, 2
	s_add_u32 s22, s22, 0x100
	s_addc_u32 s23, s23, 0
	s_add_u32 s43, s43, 0x100
	s_addc_u32 s46, s46, 0
	s_cmp_gt_u32 s47, 61
	s_barrier
	s_cbranch_scc0 .LBB0_828
	s_and_b64 vcc, exec, s[8:9]
	s_cbranch_vccz .LBB0_831
	s_barrier
